# GEMM K-loops: setprio 1 moved before opening barrier, redundant lgkmcnt(0) after it removed, setprio 0 moved after closing barrier; NSA_IN loop-head vmcnt(0) removed
# baseline (speedup 1.0000x reference)
.LBB0_162:
	ds_read_b128 v[90:93], v197
	ds_read_b128 v[94:97], v197 offset:1024
	ds_read_b128 v[98:101], v197 offset:2048
	ds_read_b128 v[102:105], v197 offset:3072
	ds_read_b128 v[146:149], v198
	ds_read_b128 v[150:153], v198 offset:1024
	ds_read_b128 v[180:183], v198 offset:2048
	ds_read_b128 v[184:187], v198 offset:3072
	s_add_u32 s36, s16, 0xfff80080
	s_addc_u32 s37, s17, -1
	s_cmp_eq_u32 s65, 28
	s_cselect_b32 s39, s15, s37
	s_cselect_b32 s38, s29, s36
	s_cselect_b32 s37, s27, s64
	s_cselect_b32 s36, s40, s41
	v_lshl_add_u64 v[212:213], s[16:17], 0, v[172:173]
	s_add_i32 m0, s44, 0xc000
	ds_read_b128 v[188:191], v199
	ds_read_b128 v[192:195], v199 offset:1024
	ds_read_b128 v[200:203], v199 offset:2048
	ds_read_b128 v[204:207], v199 offset:3072
	ds_read_b128 v[208:211], v199 offset:4096
	ds_read_b128 v[216:219], v199 offset:5120
	ds_read_b128 v[220:223], v199 offset:6144
	ds_read_b128 v[224:227], v199 offset:7168
	global_load_lds_dwordx4 v[212:213], off
	v_lshl_add_u64 v[212:213], s[16:17], 0, v[174:175]
	s_add_i32 m0, s44, 0xe000
	s_nop 0
	global_load_lds_dwordx4 v[212:213], off
	s_waitcnt vmcnt(8)
	s_waitcnt lgkmcnt(0)
	s_setprio 1
	s_barrier
	v_mfma_f32_16x16x32_bf16 v[70:73], v[90:93], v[188:191], v[70:73]
	v_mfma_f32_16x16x32_bf16 v[66:69], v[98:101], v[188:191], v[66:69]
	v_mfma_f32_16x16x32_bf16 v[54:57], v[90:93], v[200:203], v[54:57]
	v_mfma_f32_16x16x32_bf16 v[50:53], v[98:101], v[200:203], v[50:53]
	v_mfma_f32_16x16x32_bf16 v[46:49], v[90:93], v[208:211], v[46:49]
	v_mfma_f32_16x16x32_bf16 v[42:45], v[98:101], v[208:211], v[42:45]
	v_mfma_f32_16x16x32_bf16 v[38:41], v[90:93], v[220:223], v[38:41]
	v_mfma_f32_16x16x32_bf16 v[34:37], v[98:101], v[220:223], v[34:37]
	v_mfma_f32_16x16x32_bf16 v[70:73], v[94:97], v[192:195], v[70:73]
	v_mfma_f32_16x16x32_bf16 v[66:69], v[102:105], v[192:195], v[66:69]
	v_mfma_f32_16x16x32_bf16 v[54:57], v[94:97], v[204:207], v[54:57]
	v_mfma_f32_16x16x32_bf16 v[50:53], v[102:105], v[204:207], v[50:53]
	v_mfma_f32_16x16x32_bf16 v[46:49], v[94:97], v[216:219], v[46:49]
	v_mfma_f32_16x16x32_bf16 v[42:45], v[102:105], v[216:219], v[42:45]
	v_mfma_f32_16x16x32_bf16 v[38:41], v[94:97], v[224:227], v[38:41]
	v_mfma_f32_16x16x32_bf16 v[34:37], v[102:105], v[224:227], v[34:37]
	s_setprio 0
	s_setprio 1
	v_mfma_f32_16x16x32_bf16 v[142:145], v[146:149], v[188:191], v[142:145]
	v_mfma_f32_16x16x32_bf16 v[138:141], v[180:183], v[188:191], v[138:141]
	v_mfma_f32_16x16x32_bf16 v[134:137], v[146:149], v[200:203], v[134:137]
	v_mfma_f32_16x16x32_bf16 v[130:133], v[180:183], v[200:203], v[130:133]
	v_mfma_f32_16x16x32_bf16 v[126:129], v[146:149], v[208:211], v[126:129]
	v_mfma_f32_16x16x32_bf16 v[122:125], v[180:183], v[208:211], v[122:125]
	v_mfma_f32_16x16x32_bf16 v[118:121], v[146:149], v[220:223], v[118:121]
	v_mfma_f32_16x16x32_bf16 v[114:117], v[180:183], v[220:223], v[114:117]
	v_mfma_f32_16x16x32_bf16 v[142:145], v[150:153], v[192:195], v[142:145]
	v_mfma_f32_16x16x32_bf16 v[138:141], v[184:187], v[192:195], v[138:141]
	v_mfma_f32_16x16x32_bf16 v[134:137], v[150:153], v[204:207], v[134:137]
	v_mfma_f32_16x16x32_bf16 v[130:133], v[184:187], v[204:207], v[130:133]
	v_mfma_f32_16x16x32_bf16 v[126:129], v[150:153], v[216:219], v[126:129]
	v_mfma_f32_16x16x32_bf16 v[122:125], v[184:187], v[216:219], v[122:125]
	v_mfma_f32_16x16x32_bf16 v[118:121], v[150:153], v[224:227], v[118:121]
	v_mfma_f32_16x16x32_bf16 v[114:117], v[184:187], v[224:227], v[114:117]
	s_barrier
	s_setprio 0
	s_add_i32 s66, s57, s43
	v_lshl_add_u64 v[212:213], s[36:37], 0, v[156:157]
	s_mov_b32 m0, s66
	ds_read_b128 v[188:191], v199 offset:16384
	ds_read_b128 v[192:195], v199 offset:17408
	ds_read_b128 v[200:203], v199 offset:18432
	ds_read_b128 v[204:207], v199 offset:19456
	ds_read_b128 v[208:211], v199 offset:20480
	ds_read_b128 v[216:219], v199 offset:21504
	ds_read_b128 v[220:223], v199 offset:22528
	ds_read_b128 v[224:227], v199 offset:23552
	global_load_lds_dwordx4 v[212:213], off
	s_add_i32 m0, s66, 0x2000
	s_add_u32 s66, s36, 0x80000
	v_lshl_add_u64 v[214:215], s[36:37], 0, v[160:161]
	s_addc_u32 s67, s37, 0
	s_add_i32 s68, s58, s43
	global_load_lds_dwordx4 v[214:215], off
	v_lshl_add_u64 v[228:229], s[66:67], 0, v[156:157]
	s_mov_b32 m0, s68
	v_lshl_add_u64 v[230:231], s[38:39], 0, v[158:159]
	global_load_lds_dwordx4 v[228:229], off
	v_lshl_add_u64 v[228:229], s[66:67], 0, v[160:161]
	s_add_i32 m0, s68, 0x2000
	s_nop 0
	global_load_lds_dwordx4 v[228:229], off
	v_lshl_add_u64 v[228:229], s[38:39], 0, v[154:155]
	s_mov_b32 m0, s44
	s_nop 0
	global_load_lds_dwordx4 v[228:229], off
	s_mov_b32 m0, s45
	s_nop 0
	global_load_lds_dwordx4 v[230:231], off
	s_waitcnt vmcnt(8)
	s_waitcnt lgkmcnt(0)
	s_setprio 1
	s_barrier
	v_mfma_f32_16x16x32_bf16 v[30:33], v[90:93], v[188:191], v[30:33]
	v_mfma_f32_16x16x32_bf16 v[26:29], v[98:101], v[188:191], v[26:29]
	v_mfma_f32_16x16x32_bf16 v[22:25], v[90:93], v[200:203], v[22:25]
	v_mfma_f32_16x16x32_bf16 v[18:21], v[98:101], v[200:203], v[18:21]
	v_mfma_f32_16x16x32_bf16 v[14:17], v[90:93], v[208:211], v[14:17]
	v_mfma_f32_16x16x32_bf16 v[10:13], v[98:101], v[208:211], v[10:13]
	v_mfma_f32_16x16x32_bf16 v[6:9], v[90:93], v[220:223], v[6:9]
	v_mfma_f32_16x16x32_bf16 v[2:5], v[98:101], v[220:223], v[2:5]
	v_mfma_f32_16x16x32_bf16 v[30:33], v[94:97], v[192:195], v[30:33]
	v_mfma_f32_16x16x32_bf16 v[26:29], v[102:105], v[192:195], v[26:29]
	v_mfma_f32_16x16x32_bf16 v[22:25], v[94:97], v[204:207], v[22:25]
	v_mfma_f32_16x16x32_bf16 v[18:21], v[102:105], v[204:207], v[18:21]
	v_mfma_f32_16x16x32_bf16 v[14:17], v[94:97], v[216:219], v[14:17]
	v_mfma_f32_16x16x32_bf16 v[10:13], v[102:105], v[216:219], v[10:13]
	v_mfma_f32_16x16x32_bf16 v[6:9], v[94:97], v[224:227], v[6:9]
	v_mfma_f32_16x16x32_bf16 v[2:5], v[102:105], v[224:227], v[2:5]
	s_setprio 0
	s_setprio 1
	v_mfma_f32_16x16x32_bf16 v[86:89], v[146:149], v[200:203], v[86:89]
	v_mfma_f32_16x16x32_bf16 v[82:85], v[180:183], v[200:203], v[82:85]
	v_mfma_f32_16x16x32_bf16 v[78:81], v[146:149], v[208:211], v[78:81]
	v_mfma_f32_16x16x32_bf16 v[74:77], v[180:183], v[208:211], v[74:77]
	v_mfma_f32_16x16x32_bf16 v[62:65], v[146:149], v[220:223], v[62:65]
	v_mfma_f32_16x16x32_bf16 v[58:61], v[180:183], v[220:223], v[58:61]
	v_mfma_f32_16x16x32_bf16 v[90:93], v[146:149], v[188:191], v[110:113]
	v_mfma_f32_16x16x32_bf16 v[94:97], v[180:183], v[188:191], v[106:109]
	v_mfma_f32_16x16x32_bf16 v[86:89], v[150:153], v[204:207], v[86:89]
	v_mfma_f32_16x16x32_bf16 v[82:85], v[184:187], v[204:207], v[82:85]
	v_mfma_f32_16x16x32_bf16 v[78:81], v[150:153], v[216:219], v[78:81]
	v_mfma_f32_16x16x32_bf16 v[74:77], v[184:187], v[216:219], v[74:77]
	v_mfma_f32_16x16x32_bf16 v[62:65], v[150:153], v[224:227], v[62:65]
	v_mfma_f32_16x16x32_bf16 v[58:61], v[184:187], v[224:227], v[58:61]
	v_mfma_f32_16x16x32_bf16 v[90:93], v[150:153], v[192:195], v[90:93]
	v_mfma_f32_16x16x32_bf16 v[94:97], v[184:187], v[192:195], v[94:97]
	s_barrier
	s_setprio 0
	s_add_i32 s66, 0, 0x18000
	s_add_i32 s67, 0, 0x1c000
	v_add_u32_e32 v110, s66, v165
	v_add_u32_e32 v162, s67, v165
	ds_read_b128 v[98:101], v110
	ds_read_b128 v[102:105], v110 offset:1024
	ds_read_b128 v[106:109], v110 offset:2048
	ds_read_b128 v[110:113], v110 offset:3072
	ds_read_b128 v[146:149], v162
	ds_read_b128 v[150:153], v162 offset:1024
	ds_read_b128 v[180:183], v162 offset:2048
	ds_read_b128 v[184:187], v162 offset:3072
	s_add_u32 s38, s38, 0x80000
	s_addc_u32 s39, s39, 0
	s_mov_b32 m0, s47
	v_lshl_add_u64 v[232:233], s[38:39], 0, v[154:155]
	ds_read_b128 v[188:191], v199 offset:32768
	ds_read_b128 v[192:195], v199 offset:33792
	ds_read_b128 v[200:203], v199 offset:34816
	ds_read_b128 v[204:207], v199 offset:35840
	ds_read_b128 v[208:211], v199 offset:36864
	ds_read_b128 v[216:219], v199 offset:37888
	ds_read_b128 v[220:223], v199 offset:38912
	ds_read_b128 v[224:227], v199 offset:39936
	global_load_lds_dwordx4 v[232:233], off
	v_lshl_add_u64 v[232:233], s[38:39], 0, v[158:159]
	s_mov_b32 m0, s48
	s_nop 0
	global_load_lds_dwordx4 v[232:233], off
	s_waitcnt vmcnt(8)
	s_waitcnt lgkmcnt(0)
	s_setprio 1
	s_barrier
	v_mfma_f32_16x16x32_bf16 v[70:73], v[98:101], v[188:191], v[70:73]
	v_mfma_f32_16x16x32_bf16 v[66:69], v[106:109], v[188:191], v[66:69]
	v_mfma_f32_16x16x32_bf16 v[54:57], v[98:101], v[200:203], v[54:57]
	v_mfma_f32_16x16x32_bf16 v[50:53], v[106:109], v[200:203], v[50:53]
	v_mfma_f32_16x16x32_bf16 v[46:49], v[98:101], v[208:211], v[46:49]
	v_mfma_f32_16x16x32_bf16 v[42:45], v[106:109], v[208:211], v[42:45]
	v_mfma_f32_16x16x32_bf16 v[38:41], v[98:101], v[220:223], v[38:41]
	v_mfma_f32_16x16x32_bf16 v[34:37], v[106:109], v[220:223], v[34:37]
	v_mfma_f32_16x16x32_bf16 v[70:73], v[102:105], v[192:195], v[70:73]
	v_mfma_f32_16x16x32_bf16 v[66:69], v[110:113], v[192:195], v[66:69]
	v_mfma_f32_16x16x32_bf16 v[54:57], v[102:105], v[204:207], v[54:57]
	v_mfma_f32_16x16x32_bf16 v[50:53], v[110:113], v[204:207], v[50:53]
	v_mfma_f32_16x16x32_bf16 v[46:49], v[102:105], v[216:219], v[46:49]
	v_mfma_f32_16x16x32_bf16 v[42:45], v[110:113], v[216:219], v[42:45]
	v_mfma_f32_16x16x32_bf16 v[38:41], v[102:105], v[224:227], v[38:41]
	v_mfma_f32_16x16x32_bf16 v[34:37], v[110:113], v[224:227], v[34:37]
	s_setprio 0
	s_setprio 1
	v_mfma_f32_16x16x32_bf16 v[142:145], v[146:149], v[188:191], v[142:145]
	v_mfma_f32_16x16x32_bf16 v[138:141], v[180:183], v[188:191], v[138:141]
	v_mfma_f32_16x16x32_bf16 v[134:137], v[146:149], v[200:203], v[134:137]
	v_mfma_f32_16x16x32_bf16 v[130:133], v[180:183], v[200:203], v[130:133]
	v_mfma_f32_16x16x32_bf16 v[126:129], v[146:149], v[208:211], v[126:129]
	v_mfma_f32_16x16x32_bf16 v[122:125], v[180:183], v[208:211], v[122:125]
	v_mfma_f32_16x16x32_bf16 v[118:121], v[146:149], v[220:223], v[118:121]
	v_mfma_f32_16x16x32_bf16 v[114:117], v[180:183], v[220:223], v[114:117]
	v_mfma_f32_16x16x32_bf16 v[142:145], v[150:153], v[192:195], v[142:145]
	v_mfma_f32_16x16x32_bf16 v[138:141], v[184:187], v[192:195], v[138:141]
	v_mfma_f32_16x16x32_bf16 v[134:137], v[150:153], v[204:207], v[134:137]
	v_mfma_f32_16x16x32_bf16 v[130:133], v[184:187], v[204:207], v[130:133]
	v_mfma_f32_16x16x32_bf16 v[126:129], v[150:153], v[216:219], v[126:129]
	v_mfma_f32_16x16x32_bf16 v[122:125], v[184:187], v[216:219], v[122:125]
	v_mfma_f32_16x16x32_bf16 v[118:121], v[150:153], v[224:227], v[118:121]
	v_mfma_f32_16x16x32_bf16 v[114:117], v[184:187], v[224:227], v[114:117]
	s_barrier
	s_setprio 0
	s_add_i32 s38, s66, s43
	v_lshl_add_u64 v[212:213], v[212:213], 0, s[18:19]
	s_mov_b32 m0, s38
	ds_read_b128 v[188:191], v199 offset:49152
	ds_read_b128 v[192:195], v199 offset:50176
	ds_read_b128 v[200:203], v199 offset:51200
	ds_read_b128 v[204:207], v199 offset:52224
	ds_read_b128 v[208:211], v199 offset:53248
	ds_read_b128 v[216:219], v199 offset:54272
	ds_read_b128 v[220:223], v199 offset:55296
	ds_read_b128 v[224:227], v199 offset:56320
	global_load_lds_dwordx4 v[212:213], off
	s_add_i32 m0, s38, 0x2000
	s_add_u32 s36, s36, 0x80080
	v_lshl_add_u64 v[212:213], v[214:215], 0, s[18:19]
	s_addc_u32 s37, s37, 0
	s_add_i32 s38, s67, s43
	global_load_lds_dwordx4 v[212:213], off
	v_lshl_add_u64 v[212:213], s[36:37], 0, v[156:157]
	s_mov_b32 m0, s38
	s_nop 0
	global_load_lds_dwordx4 v[212:213], off
	v_lshl_add_u64 v[212:213], s[36:37], 0, v[160:161]
	s_add_i32 m0, s38, 0x2000
	s_nop 0
	global_load_lds_dwordx4 v[212:213], off
	v_lshl_add_u64 v[212:213], v[228:229], 0, s[18:19]
	s_mov_b32 m0, s52
	s_nop 0
	global_load_lds_dwordx4 v[212:213], off
	v_lshl_add_u64 v[212:213], v[230:231], 0, s[18:19]
	s_mov_b32 m0, s53
	s_nop 0
	global_load_lds_dwordx4 v[212:213], off
	s_waitcnt vmcnt(8)
	s_waitcnt lgkmcnt(0)
	s_setprio 1
	s_barrier
	v_mfma_f32_16x16x32_bf16 v[30:33], v[98:101], v[188:191], v[30:33]
	v_mfma_f32_16x16x32_bf16 v[26:29], v[106:109], v[188:191], v[26:29]
	v_mfma_f32_16x16x32_bf16 v[22:25], v[98:101], v[200:203], v[22:25]
	v_mfma_f32_16x16x32_bf16 v[18:21], v[106:109], v[200:203], v[18:21]
	v_mfma_f32_16x16x32_bf16 v[14:17], v[98:101], v[208:211], v[14:17]
	v_mfma_f32_16x16x32_bf16 v[10:13], v[106:109], v[208:211], v[10:13]
	v_mfma_f32_16x16x32_bf16 v[6:9], v[98:101], v[220:223], v[6:9]
	v_mfma_f32_16x16x32_bf16 v[2:5], v[106:109], v[220:223], v[2:5]
	v_mfma_f32_16x16x32_bf16 v[30:33], v[102:105], v[192:195], v[30:33]
	v_mfma_f32_16x16x32_bf16 v[26:29], v[110:113], v[192:195], v[26:29]
	v_mfma_f32_16x16x32_bf16 v[22:25], v[102:105], v[204:207], v[22:25]
	v_mfma_f32_16x16x32_bf16 v[18:21], v[110:113], v[204:207], v[18:21]
	v_mfma_f32_16x16x32_bf16 v[14:17], v[102:105], v[216:219], v[14:17]
	v_mfma_f32_16x16x32_bf16 v[10:13], v[110:113], v[216:219], v[10:13]
	v_mfma_f32_16x16x32_bf16 v[6:9], v[102:105], v[224:227], v[6:9]
	v_mfma_f32_16x16x32_bf16 v[2:5], v[110:113], v[224:227], v[2:5]
	s_setprio 0
	s_setprio 1
	v_mfma_f32_16x16x32_bf16 v[90:93], v[146:149], v[188:191], v[90:93]
	v_mfma_f32_16x16x32_bf16 v[110:113], v[150:153], v[192:195], v[90:93]
	v_mfma_f32_16x16x32_bf16 v[90:93], v[180:183], v[188:191], v[94:97]
	v_mfma_f32_16x16x32_bf16 v[86:89], v[146:149], v[200:203], v[86:89]
	v_mfma_f32_16x16x32_bf16 v[82:85], v[180:183], v[200:203], v[82:85]
	v_mfma_f32_16x16x32_bf16 v[78:81], v[146:149], v[208:211], v[78:81]
	v_mfma_f32_16x16x32_bf16 v[74:77], v[180:183], v[208:211], v[74:77]
	v_mfma_f32_16x16x32_bf16 v[62:65], v[146:149], v[220:223], v[62:65]
	v_mfma_f32_16x16x32_bf16 v[58:61], v[180:183], v[220:223], v[58:61]
	v_mfma_f32_16x16x32_bf16 v[106:109], v[184:187], v[192:195], v[90:93]
	v_mfma_f32_16x16x32_bf16 v[86:89], v[150:153], v[204:207], v[86:89]
	v_mfma_f32_16x16x32_bf16 v[82:85], v[184:187], v[204:207], v[82:85]
	v_mfma_f32_16x16x32_bf16 v[78:81], v[150:153], v[216:219], v[78:81]
	v_mfma_f32_16x16x32_bf16 v[74:77], v[184:187], v[216:219], v[74:77]
	v_mfma_f32_16x16x32_bf16 v[62:65], v[150:153], v[224:227], v[62:65]
	v_mfma_f32_16x16x32_bf16 v[58:61], v[184:187], v[224:227], v[58:61]
	s_barrier
	s_setprio 0
	s_add_i32 s65, s65, 2
	s_add_u32 s16, s16, 0x100
	s_addc_u32 s17, s17, 0
	s_add_u32 s41, s41, 0x100
	s_addc_u32 s64, s64, 0
	s_cmp_gt_u32 s65, 29
	s_cbranch_scc0 .LBB0_162
	s_and_b64 vcc, exec, s[20:21]
	s_cbranch_vccz .LBB0_165
	s_barrier

.LBB0_428:
	ds_read_b128 v[150:153], v146
	ds_read_b128 v[154:157], v146 offset:1024
	ds_read_b128 v[158:161], v146 offset:2048
	ds_read_b128 v[162:165], v146 offset:3072
	ds_read_b128 v[166:169], v147
	ds_read_b128 v[170:173], v147 offset:1024
	ds_read_b128 v[174:177], v147 offset:2048
	ds_read_b128 v[178:181], v147 offset:3072
	s_add_u32 s30, s0, 0xfff80080
	s_addc_u32 s31, s1, -1
	s_cmp_eq_u32 s59, 28
	s_cselect_b32 s35, s25, s31
	s_cselect_b32 s34, s55, s30
	s_cselect_b32 s31, s27, s58
	s_cselect_b32 s30, s56, s57
	v_lshl_add_u64 v[142:143], s[0:1], 0, v[138:139]
	s_add_i32 m0, s39, 0xc000
	ds_read_b128 v[182:185], v148
	ds_read_b128 v[186:189], v148 offset:1024
	ds_read_b128 v[190:193], v148 offset:2048
	ds_read_b128 v[194:197], v148 offset:3072
	ds_read_b128 v[198:201], v148 offset:4096
	ds_read_b128 v[202:205], v148 offset:5120
	ds_read_b128 v[206:209], v148 offset:6144
	ds_read_b128 v[210:213], v148 offset:7168
	global_load_lds_dwordx4 v[142:143], off
	v_lshl_add_u64 v[142:143], s[0:1], 0, v[140:141]
	s_add_i32 m0, s39, 0xe000
	s_nop 0
	global_load_lds_dwordx4 v[142:143], off
	s_waitcnt vmcnt(8)
	s_waitcnt lgkmcnt(0)
	s_setprio 1
	s_barrier
	v_mfma_f32_16x16x32_bf16 v[94:97], v[150:153], v[182:185], v[94:97]
	v_mfma_f32_16x16x32_bf16 v[86:89], v[158:161], v[182:185], v[86:89]
	v_mfma_f32_16x16x32_bf16 v[66:69], v[150:153], v[190:193], v[66:69]
	v_mfma_f32_16x16x32_bf16 v[50:53], v[158:161], v[190:193], v[50:53]
	v_mfma_f32_16x16x32_bf16 v[46:49], v[150:153], v[198:201], v[46:49]
	v_mfma_f32_16x16x32_bf16 v[42:45], v[158:161], v[198:201], v[42:45]
	v_mfma_f32_16x16x32_bf16 v[38:41], v[150:153], v[206:209], v[38:41]
	v_mfma_f32_16x16x32_bf16 v[34:37], v[158:161], v[206:209], v[34:37]
	v_mfma_f32_16x16x32_bf16 v[94:97], v[154:157], v[186:189], v[94:97]
	v_mfma_f32_16x16x32_bf16 v[86:89], v[162:165], v[186:189], v[86:89]
	v_mfma_f32_16x16x32_bf16 v[66:69], v[154:157], v[194:197], v[66:69]
	v_mfma_f32_16x16x32_bf16 v[50:53], v[162:165], v[194:197], v[50:53]
	v_mfma_f32_16x16x32_bf16 v[46:49], v[154:157], v[202:205], v[46:49]
	v_mfma_f32_16x16x32_bf16 v[42:45], v[162:165], v[202:205], v[42:45]
	v_mfma_f32_16x16x32_bf16 v[38:41], v[154:157], v[210:213], v[38:41]
	v_mfma_f32_16x16x32_bf16 v[34:37], v[162:165], v[210:213], v[34:37]
	s_setprio 0
	s_setprio 1
	v_mfma_f32_16x16x32_bf16 v[126:129], v[166:169], v[182:185], v[126:129]
	v_mfma_f32_16x16x32_bf16 v[122:125], v[174:177], v[182:185], v[122:125]
	v_mfma_f32_16x16x32_bf16 v[118:121], v[166:169], v[190:193], v[118:121]
	v_mfma_f32_16x16x32_bf16 v[114:117], v[174:177], v[190:193], v[114:117]
	v_mfma_f32_16x16x32_bf16 v[110:113], v[166:169], v[198:201], v[110:113]
	v_mfma_f32_16x16x32_bf16 v[106:109], v[174:177], v[198:201], v[106:109]
	v_mfma_f32_16x16x32_bf16 v[102:105], v[166:169], v[206:209], v[102:105]
	v_mfma_f32_16x16x32_bf16 v[98:101], v[174:177], v[206:209], v[98:101]
	v_mfma_f32_16x16x32_bf16 v[126:129], v[170:173], v[186:189], v[126:129]
	v_mfma_f32_16x16x32_bf16 v[122:125], v[178:181], v[186:189], v[122:125]
	v_mfma_f32_16x16x32_bf16 v[118:121], v[170:173], v[194:197], v[118:121]
	v_mfma_f32_16x16x32_bf16 v[114:117], v[178:181], v[194:197], v[114:117]
	v_mfma_f32_16x16x32_bf16 v[110:113], v[170:173], v[202:205], v[110:113]
	v_mfma_f32_16x16x32_bf16 v[106:109], v[178:181], v[202:205], v[106:109]
	v_mfma_f32_16x16x32_bf16 v[102:105], v[170:173], v[210:213], v[102:105]
	v_mfma_f32_16x16x32_bf16 v[98:101], v[178:181], v[210:213], v[98:101]
	s_barrier
	s_setprio 0
	s_add_i32 s60, s47, s38
	v_lshl_add_u64 v[142:143], s[30:31], 0, v[130:131]
	s_mov_b32 m0, s60
	ds_read_b128 v[182:185], v148 offset:16384
	ds_read_b128 v[186:189], v148 offset:17408
	ds_read_b128 v[190:193], v148 offset:18432
	ds_read_b128 v[194:197], v148 offset:19456
	ds_read_b128 v[198:201], v148 offset:20480
	ds_read_b128 v[202:205], v148 offset:21504
	ds_read_b128 v[206:209], v148 offset:22528
	ds_read_b128 v[210:213], v148 offset:23552
	global_load_lds_dwordx4 v[142:143], off
	s_add_i32 m0, s60, 0x2000
	s_add_u32 s60, s30, 0x80000
	v_lshl_add_u64 v[214:215], s[30:31], 0, v[132:133]
	s_addc_u32 s61, s31, 0
	s_add_i32 s62, s48, s38
	global_load_lds_dwordx4 v[214:215], off
	v_lshl_add_u64 v[216:217], s[60:61], 0, v[130:131]
	s_mov_b32 m0, s62
	v_lshl_add_u64 v[218:219], s[34:35], 0, v[132:133]
	global_load_lds_dwordx4 v[216:217], off
	v_lshl_add_u64 v[216:217], s[60:61], 0, v[132:133]
	s_add_i32 m0, s62, 0x2000
	s_nop 0
	global_load_lds_dwordx4 v[216:217], off
	v_lshl_add_u64 v[216:217], s[34:35], 0, v[130:131]
	s_mov_b32 m0, s39
	s_nop 0
	global_load_lds_dwordx4 v[216:217], off
	s_mov_b32 m0, s40
	s_nop 0
	global_load_lds_dwordx4 v[218:219], off
	s_waitcnt vmcnt(8)
	s_waitcnt lgkmcnt(0)
	s_setprio 1
	s_barrier
	v_mfma_f32_16x16x32_bf16 v[30:33], v[150:153], v[182:185], v[30:33]
	v_mfma_f32_16x16x32_bf16 v[26:29], v[158:161], v[182:185], v[26:29]
	v_mfma_f32_16x16x32_bf16 v[22:25], v[150:153], v[190:193], v[22:25]
	v_mfma_f32_16x16x32_bf16 v[18:21], v[158:161], v[190:193], v[18:21]
	v_mfma_f32_16x16x32_bf16 v[14:17], v[150:153], v[198:201], v[14:17]
	v_mfma_f32_16x16x32_bf16 v[10:13], v[158:161], v[198:201], v[10:13]
	v_mfma_f32_16x16x32_bf16 v[6:9], v[150:153], v[206:209], v[6:9]
	v_mfma_f32_16x16x32_bf16 v[2:5], v[158:161], v[206:209], v[2:5]
	v_mfma_f32_16x16x32_bf16 v[30:33], v[154:157], v[186:189], v[30:33]
	v_mfma_f32_16x16x32_bf16 v[26:29], v[162:165], v[186:189], v[26:29]
	v_mfma_f32_16x16x32_bf16 v[22:25], v[154:157], v[194:197], v[22:25]
	v_mfma_f32_16x16x32_bf16 v[18:21], v[162:165], v[194:197], v[18:21]
	v_mfma_f32_16x16x32_bf16 v[14:17], v[154:157], v[202:205], v[14:17]
	v_mfma_f32_16x16x32_bf16 v[10:13], v[162:165], v[202:205], v[10:13]
	v_mfma_f32_16x16x32_bf16 v[6:9], v[154:157], v[210:213], v[6:9]
	v_mfma_f32_16x16x32_bf16 v[2:5], v[162:165], v[210:213], v[2:5]
	s_setprio 0
	s_setprio 1
	v_mfma_f32_16x16x32_bf16 v[90:93], v[166:169], v[182:185], v[90:93]
	v_mfma_f32_16x16x32_bf16 v[82:85], v[174:177], v[182:185], v[82:85]
	v_mfma_f32_16x16x32_bf16 v[78:81], v[166:169], v[190:193], v[78:81]
	v_mfma_f32_16x16x32_bf16 v[74:77], v[174:177], v[190:193], v[74:77]
	v_mfma_f32_16x16x32_bf16 v[70:73], v[166:169], v[198:201], v[70:73]
	v_mfma_f32_16x16x32_bf16 v[62:65], v[174:177], v[198:201], v[62:65]
	v_mfma_f32_16x16x32_bf16 v[58:61], v[166:169], v[206:209], v[58:61]
	v_mfma_f32_16x16x32_bf16 v[54:57], v[174:177], v[206:209], v[54:57]
	v_mfma_f32_16x16x32_bf16 v[90:93], v[170:173], v[186:189], v[90:93]
	v_mfma_f32_16x16x32_bf16 v[82:85], v[178:181], v[186:189], v[82:85]
	v_mfma_f32_16x16x32_bf16 v[78:81], v[170:173], v[194:197], v[78:81]
	v_mfma_f32_16x16x32_bf16 v[74:77], v[178:181], v[194:197], v[74:77]
	v_mfma_f32_16x16x32_bf16 v[70:73], v[170:173], v[202:205], v[70:73]
	v_mfma_f32_16x16x32_bf16 v[62:65], v[178:181], v[202:205], v[62:65]
	v_mfma_f32_16x16x32_bf16 v[58:61], v[170:173], v[210:213], v[58:61]
	v_mfma_f32_16x16x32_bf16 v[54:57], v[178:181], v[210:213], v[54:57]
	s_barrier
	s_setprio 0
	s_add_i32 s60, 0, 0x18000
	v_add_u32_e32 v134, s60, v144
	s_add_i32 s61, 0, 0x1c000
	ds_read_b128 v[150:153], v134
	ds_read_b128 v[154:157], v134 offset:1024
	ds_read_b128 v[158:161], v134 offset:2048
	ds_read_b128 v[162:165], v134 offset:3072
	v_add_u32_e32 v134, s61, v144
	ds_read_b128 v[166:169], v134
	ds_read_b128 v[170:173], v134 offset:1024
	ds_read_b128 v[174:177], v134 offset:2048
	ds_read_b128 v[178:181], v134 offset:3072
	s_add_u32 s34, s34, 0x80000
	s_addc_u32 s35, s35, 0
	s_mov_b32 m0, s41
	v_lshl_add_u64 v[220:221], s[34:35], 0, v[130:131]
	ds_read_b128 v[182:185], v148 offset:32768
	ds_read_b128 v[186:189], v148 offset:33792
	ds_read_b128 v[190:193], v148 offset:34816
	ds_read_b128 v[194:197], v148 offset:35840
	ds_read_b128 v[198:201], v148 offset:36864
	ds_read_b128 v[202:205], v148 offset:37888
	ds_read_b128 v[206:209], v148 offset:38912
	ds_read_b128 v[210:213], v148 offset:39936
	global_load_lds_dwordx4 v[220:221], off
	v_lshl_add_u64 v[220:221], s[34:35], 0, v[132:133]
	s_mov_b32 m0, s42
	s_nop 0
	global_load_lds_dwordx4 v[220:221], off
	s_waitcnt vmcnt(8)
	s_waitcnt lgkmcnt(0)
	s_setprio 1
	s_barrier
	v_mfma_f32_16x16x32_bf16 v[94:97], v[150:153], v[182:185], v[94:97]
	v_mfma_f32_16x16x32_bf16 v[86:89], v[158:161], v[182:185], v[86:89]
	v_mfma_f32_16x16x32_bf16 v[66:69], v[150:153], v[190:193], v[66:69]
	v_mfma_f32_16x16x32_bf16 v[50:53], v[158:161], v[190:193], v[50:53]
	v_mfma_f32_16x16x32_bf16 v[46:49], v[150:153], v[198:201], v[46:49]
	v_mfma_f32_16x16x32_bf16 v[42:45], v[158:161], v[198:201], v[42:45]
	v_mfma_f32_16x16x32_bf16 v[38:41], v[150:153], v[206:209], v[38:41]
	v_mfma_f32_16x16x32_bf16 v[34:37], v[158:161], v[206:209], v[34:37]
	v_mfma_f32_16x16x32_bf16 v[94:97], v[154:157], v[186:189], v[94:97]
	v_mfma_f32_16x16x32_bf16 v[86:89], v[162:165], v[186:189], v[86:89]
	v_mfma_f32_16x16x32_bf16 v[66:69], v[154:157], v[194:197], v[66:69]
	v_mfma_f32_16x16x32_bf16 v[50:53], v[162:165], v[194:197], v[50:53]
	v_mfma_f32_16x16x32_bf16 v[46:49], v[154:157], v[202:205], v[46:49]
	v_mfma_f32_16x16x32_bf16 v[42:45], v[162:165], v[202:205], v[42:45]
	v_mfma_f32_16x16x32_bf16 v[38:41], v[154:157], v[210:213], v[38:41]
	v_mfma_f32_16x16x32_bf16 v[34:37], v[162:165], v[210:213], v[34:37]
	s_setprio 0
	s_setprio 1
	v_mfma_f32_16x16x32_bf16 v[126:129], v[166:169], v[182:185], v[126:129]
	v_mfma_f32_16x16x32_bf16 v[122:125], v[174:177], v[182:185], v[122:125]
	v_mfma_f32_16x16x32_bf16 v[118:121], v[166:169], v[190:193], v[118:121]
	v_mfma_f32_16x16x32_bf16 v[114:117], v[174:177], v[190:193], v[114:117]
	v_mfma_f32_16x16x32_bf16 v[110:113], v[166:169], v[198:201], v[110:113]
	v_mfma_f32_16x16x32_bf16 v[106:109], v[174:177], v[198:201], v[106:109]
	v_mfma_f32_16x16x32_bf16 v[102:105], v[166:169], v[206:209], v[102:105]
	v_mfma_f32_16x16x32_bf16 v[98:101], v[174:177], v[206:209], v[98:101]
	v_mfma_f32_16x16x32_bf16 v[126:129], v[170:173], v[186:189], v[126:129]
	v_mfma_f32_16x16x32_bf16 v[122:125], v[178:181], v[186:189], v[122:125]
	v_mfma_f32_16x16x32_bf16 v[118:121], v[170:173], v[194:197], v[118:121]
	v_mfma_f32_16x16x32_bf16 v[114:117], v[178:181], v[194:197], v[114:117]
	v_mfma_f32_16x16x32_bf16 v[110:113], v[170:173], v[202:205], v[110:113]
	v_mfma_f32_16x16x32_bf16 v[106:109], v[178:181], v[202:205], v[106:109]
	v_mfma_f32_16x16x32_bf16 v[102:105], v[170:173], v[210:213], v[102:105]
	v_mfma_f32_16x16x32_bf16 v[98:101], v[178:181], v[210:213], v[98:101]
	s_barrier
	s_setprio 0
	s_add_i32 s34, s60, s38
	v_lshl_add_u64 v[142:143], v[142:143], 0, s[6:7]
	s_mov_b32 m0, s34
	ds_read_b128 v[182:185], v148 offset:49152
	ds_read_b128 v[186:189], v148 offset:50176
	ds_read_b128 v[190:193], v148 offset:51200
	ds_read_b128 v[194:197], v148 offset:52224
	ds_read_b128 v[198:201], v148 offset:53248
	ds_read_b128 v[202:205], v148 offset:54272
	ds_read_b128 v[206:209], v148 offset:55296
	ds_read_b128 v[210:213], v148 offset:56320
	global_load_lds_dwordx4 v[142:143], off
	s_add_i32 m0, s34, 0x2000
	s_add_u32 s30, s30, 0x80080
	v_lshl_add_u64 v[142:143], v[214:215], 0, s[6:7]
	s_addc_u32 s31, s31, 0
	s_add_i32 s34, s61, s38
	global_load_lds_dwordx4 v[142:143], off
	v_lshl_add_u64 v[142:143], s[30:31], 0, v[130:131]
	s_mov_b32 m0, s34
	s_nop 0
	global_load_lds_dwordx4 v[142:143], off
	v_lshl_add_u64 v[142:143], s[30:31], 0, v[132:133]
	s_add_i32 m0, s34, 0x2000
	s_nop 0
	global_load_lds_dwordx4 v[142:143], off
	v_lshl_add_u64 v[142:143], v[216:217], 0, s[6:7]
	s_mov_b32 m0, s44
	s_nop 0
	global_load_lds_dwordx4 v[142:143], off
	v_lshl_add_u64 v[142:143], v[218:219], 0, s[6:7]
	s_mov_b32 m0, s45
	s_nop 0
	global_load_lds_dwordx4 v[142:143], off
	s_waitcnt vmcnt(8)
	s_waitcnt lgkmcnt(0)
	s_setprio 1
	s_barrier
	v_mfma_f32_16x16x32_bf16 v[30:33], v[150:153], v[182:185], v[30:33]
	v_mfma_f32_16x16x32_bf16 v[26:29], v[158:161], v[182:185], v[26:29]
	v_mfma_f32_16x16x32_bf16 v[22:25], v[150:153], v[190:193], v[22:25]
	v_mfma_f32_16x16x32_bf16 v[18:21], v[158:161], v[190:193], v[18:21]
	v_mfma_f32_16x16x32_bf16 v[14:17], v[150:153], v[198:201], v[14:17]
	v_mfma_f32_16x16x32_bf16 v[10:13], v[158:161], v[198:201], v[10:13]
	v_mfma_f32_16x16x32_bf16 v[6:9], v[150:153], v[206:209], v[6:9]
	v_mfma_f32_16x16x32_bf16 v[2:5], v[158:161], v[206:209], v[2:5]
	v_mfma_f32_16x16x32_bf16 v[30:33], v[154:157], v[186:189], v[30:33]
	v_mfma_f32_16x16x32_bf16 v[26:29], v[162:165], v[186:189], v[26:29]
	v_mfma_f32_16x16x32_bf16 v[22:25], v[154:157], v[194:197], v[22:25]
	v_mfma_f32_16x16x32_bf16 v[18:21], v[162:165], v[194:197], v[18:21]
	v_mfma_f32_16x16x32_bf16 v[14:17], v[154:157], v[202:205], v[14:17]
	v_mfma_f32_16x16x32_bf16 v[10:13], v[162:165], v[202:205], v[10:13]
	v_mfma_f32_16x16x32_bf16 v[6:9], v[154:157], v[210:213], v[6:9]
	v_mfma_f32_16x16x32_bf16 v[2:5], v[162:165], v[210:213], v[2:5]
	s_setprio 0
	s_setprio 1
	v_mfma_f32_16x16x32_bf16 v[90:93], v[166:169], v[182:185], v[90:93]
	v_mfma_f32_16x16x32_bf16 v[82:85], v[174:177], v[182:185], v[82:85]
	v_mfma_f32_16x16x32_bf16 v[78:81], v[166:169], v[190:193], v[78:81]
	v_mfma_f32_16x16x32_bf16 v[74:77], v[174:177], v[190:193], v[74:77]
	v_mfma_f32_16x16x32_bf16 v[70:73], v[166:169], v[198:201], v[70:73]
	v_mfma_f32_16x16x32_bf16 v[62:65], v[174:177], v[198:201], v[62:65]
	v_mfma_f32_16x16x32_bf16 v[58:61], v[166:169], v[206:209], v[58:61]
	v_mfma_f32_16x16x32_bf16 v[54:57], v[174:177], v[206:209], v[54:57]
	v_mfma_f32_16x16x32_bf16 v[90:93], v[170:173], v[186:189], v[90:93]
	v_mfma_f32_16x16x32_bf16 v[82:85], v[178:181], v[186:189], v[82:85]
	v_mfma_f32_16x16x32_bf16 v[78:81], v[170:173], v[194:197], v[78:81]
	v_mfma_f32_16x16x32_bf16 v[74:77], v[178:181], v[194:197], v[74:77]
	v_mfma_f32_16x16x32_bf16 v[70:73], v[170:173], v[202:205], v[70:73]
	v_mfma_f32_16x16x32_bf16 v[62:65], v[178:181], v[202:205], v[62:65]
	v_mfma_f32_16x16x32_bf16 v[58:61], v[170:173], v[210:213], v[58:61]
	v_mfma_f32_16x16x32_bf16 v[54:57], v[178:181], v[210:213], v[54:57]
	s_barrier
	s_setprio 0
	s_add_i32 s59, s59, 2
	s_add_u32 s0, s0, 0x100
	s_addc_u32 s1, s1, 0
	s_add_u32 s57, s57, 0x100
	s_addc_u32 s58, s58, 0
	s_cmp_gt_u32 s59, 29
	s_cbranch_scc0 .LBB0_428
	v_lshl_add_u32 v142, s54, 8, v1
	s_cmp_lt_i32 s53, 8
	s_mov_b64 s[0:1], -1
	s_cbranch_scc0 .LBB0_431
	s_lshl_b32 s0, s53, 8
	s_and_b32 s0, s0, 0x100
	v_ashrrev_i32_e32 v143, 31, v142
	v_or_b32_e32 v134, s0, v145
	v_lshlrev_b64 v[150:151], 11, v[142:143]
	v_lshl_add_u64 v[150:151], s[4:5], 0, v[150:151]
	v_lshlrev_b32_e32 v134, 2, v134
	v_lshl_add_u64 v[150:151], v[150:151], 0, v[134:135]
	global_store_dwordx4 v[150:151], v[94:97], off
	global_store_dwordx4 v[150:151], v[86:89], off offset:64
	global_store_dwordx4 v[150:151], v[126:129], off offset:512
	global_store_dwordx4 v[150:151], v[122:125], off offset:576
	s_mov_b64 s[0:1], 0
	s_nop 0
	v_or_b32_e32 v122, 16, v142
	v_ashrrev_i32_e32 v123, 31, v122
	v_lshlrev_b64 v[122:123], 11, v[122:123]
	v_lshl_add_u64 v[122:123], s[4:5], 0, v[122:123]
	v_lshl_add_u64 v[122:123], v[122:123], 0, v[134:135]
	global_store_dwordx4 v[122:123], v[66:69], off
	global_store_dwordx4 v[122:123], v[50:53], off offset:64
	global_store_dwordx4 v[122:123], v[118:121], off offset:512
	global_store_dwordx4 v[122:123], v[114:117], off offset:576
	s_nop 1
	v_or_b32_e32 v114, 32, v142
	v_ashrrev_i32_e32 v115, 31, v114
	v_lshlrev_b64 v[114:115], 11, v[114:115]
	v_lshl_add_u64 v[114:115], s[4:5], 0, v[114:115]
	v_lshl_add_u64 v[114:115], v[114:115], 0, v[134:135]
	global_store_dwordx4 v[114:115], v[46:49], off
	global_store_dwordx4 v[114:115], v[42:45], off offset:64
	global_store_dwordx4 v[114:115], v[110:113], off offset:512
	global_store_dwordx4 v[114:115], v[106:109], off offset:576
	s_nop 1
	v_or_b32_e32 v106, 48, v142
	v_ashrrev_i32_e32 v107, 31, v106
	v_lshlrev_b64 v[106:107], 11, v[106:107]
	v_lshl_add_u64 v[106:107], s[4:5], 0, v[106:107]
	v_lshl_add_u64 v[106:107], v[106:107], 0, v[134:135]
	global_store_dwordx4 v[106:107], v[38:41], off
	global_store_dwordx4 v[106:107], v[34:37], off offset:64
	global_store_dwordx4 v[106:107], v[102:105], off offset:512
	global_store_dwordx4 v[106:107], v[98:101], off offset:576
	s_nop 1
	v_add_co_u32_e32 v100, vcc, s49, v150
	v_lshl_add_u64 v[98:99], v[150:151], 0, s[16:17]
	s_nop 0
	v_addc_co_u32_e32 v101, vcc, 0, v151, vcc
	global_store_dwordx4 v[100:101], v[30:33], off
	global_store_dwordx4 v[98:99], v[26:29], off offset:64
	global_store_dwordx4 v[98:99], v[90:93], off offset:512
	global_store_dwordx4 v[98:99], v[82:85], off offset:576
	s_nop 1
	v_add_co_u32_e32 v84, vcc, s50, v150
	v_lshl_add_u64 v[82:83], v[150:151], 0, s[18:19]
	s_nop 0
	v_addc_co_u32_e32 v85, vcc, 0, v151, vcc
	global_store_dwordx4 v[84:85], v[22:25], off
	global_store_dwordx4 v[82:83], v[18:21], off offset:64
	global_store_dwordx4 v[82:83], v[78:81], off offset:512
	global_store_dwordx4 v[82:83], v[74:77], off offset:576
	s_nop 1
	v_add_co_u32_e32 v76, vcc, s51, v150
	v_lshl_add_u64 v[74:75], v[150:151], 0, s[20:21]
	s_nop 0
	v_addc_co_u32_e32 v77, vcc, 0, v151, vcc
	global_store_dwordx4 v[76:77], v[14:17], off
	global_store_dwordx4 v[74:75], v[10:13], off offset:64
	global_store_dwordx4 v[74:75], v[70:73], off offset:512
	global_store_dwordx4 v[74:75], v[62:65], off offset:576
	s_nop 1
	v_add_co_u32_e32 v64, vcc, 0x58000, v150
	v_lshl_add_u64 v[62:63], v[150:151], 0, s[22:23]
	s_nop 0
	v_addc_co_u32_e32 v65, vcc, 0, v151, vcc
	global_store_dwordx4 v[64:65], v[6:9], off
	global_store_dwordx4 v[62:63], v[2:5], off offset:64
	global_store_dwordx4 v[62:63], v[58:61], off offset:512
	global_store_dwordx4 v[62:63], v[54:57], off offset:576

.LBB0_1346:
	ds_read_b128 v[154:157], v150
	ds_read_b128 v[158:161], v150 offset:1024
	ds_read_b128 v[162:165], v150 offset:2048
	ds_read_b128 v[166:169], v150 offset:3072
	ds_read_b128 v[170:173], v151
	ds_read_b128 v[174:177], v151 offset:1024
	ds_read_b128 v[178:181], v151 offset:2048
	ds_read_b128 v[182:185], v151 offset:3072
	s_add_u32 s34, s30, 0xfff80080
	s_addc_u32 s35, s31, -1
	s_cmp_eq_u32 s59, 28
	s_cselect_b32 s37, s23, s35
	s_cselect_b32 s36, s55, s34
	s_cselect_b32 s35, s21, s58
	s_cselect_b32 s34, s56, s57
	v_lshl_add_u64 v[146:147], s[30:31], 0, v[138:139]
	s_add_i32 m0, s29, 0xc000
	ds_read_b128 v[186:189], v152
	ds_read_b128 v[190:193], v152 offset:1024
	ds_read_b128 v[194:197], v152 offset:2048
	ds_read_b128 v[198:201], v152 offset:3072
	ds_read_b128 v[202:205], v152 offset:4096
	ds_read_b128 v[206:209], v152 offset:5120
	ds_read_b128 v[210:213], v152 offset:6144
	ds_read_b128 v[214:217], v152 offset:7168
	global_load_lds_dwordx4 v[146:147], off
	v_lshl_add_u64 v[146:147], s[30:31], 0, v[140:141]
	s_add_i32 m0, s29, 0xe000
	s_nop 0
	global_load_lds_dwordx4 v[146:147], off
	s_waitcnt vmcnt(8)
	s_waitcnt lgkmcnt(0)
	s_setprio 1
	s_barrier
	v_mfma_f32_16x16x32_bf16 v[126:129], v[154:157], v[186:189], v[126:129]
	v_mfma_f32_16x16x32_bf16 v[122:125], v[162:165], v[186:189], v[122:125]
	v_mfma_f32_16x16x32_bf16 v[118:121], v[154:157], v[194:197], v[118:121]
	v_mfma_f32_16x16x32_bf16 v[110:113], v[162:165], v[194:197], v[110:113]
	v_mfma_f32_16x16x32_bf16 v[102:105], v[154:157], v[202:205], v[102:105]
	v_mfma_f32_16x16x32_bf16 v[94:97], v[162:165], v[202:205], v[94:97]
	v_mfma_f32_16x16x32_bf16 v[86:89], v[154:157], v[210:213], v[86:89]
	v_mfma_f32_16x16x32_bf16 v[78:81], v[162:165], v[210:213], v[78:81]
	v_mfma_f32_16x16x32_bf16 v[126:129], v[158:161], v[190:193], v[126:129]
	v_mfma_f32_16x16x32_bf16 v[122:125], v[166:169], v[190:193], v[122:125]
	v_mfma_f32_16x16x32_bf16 v[118:121], v[158:161], v[198:201], v[118:121]
	v_mfma_f32_16x16x32_bf16 v[110:113], v[166:169], v[198:201], v[110:113]
	v_mfma_f32_16x16x32_bf16 v[102:105], v[158:161], v[206:209], v[102:105]
	v_mfma_f32_16x16x32_bf16 v[94:97], v[166:169], v[206:209], v[94:97]
	v_mfma_f32_16x16x32_bf16 v[86:89], v[158:161], v[214:217], v[86:89]
	v_mfma_f32_16x16x32_bf16 v[78:81], v[166:169], v[214:217], v[78:81]
	s_setprio 0
	s_setprio 1
	v_mfma_f32_16x16x32_bf16 v[114:117], v[170:173], v[186:189], v[114:117]
	v_mfma_f32_16x16x32_bf16 v[106:109], v[178:181], v[186:189], v[106:109]
	v_mfma_f32_16x16x32_bf16 v[98:101], v[170:173], v[194:197], v[98:101]
	v_mfma_f32_16x16x32_bf16 v[90:93], v[178:181], v[194:197], v[90:93]
	v_mfma_f32_16x16x32_bf16 v[82:85], v[170:173], v[202:205], v[82:85]
	v_mfma_f32_16x16x32_bf16 v[74:77], v[178:181], v[202:205], v[74:77]
	v_mfma_f32_16x16x32_bf16 v[70:73], v[170:173], v[210:213], v[70:73]
	v_mfma_f32_16x16x32_bf16 v[66:69], v[178:181], v[210:213], v[66:69]
	v_mfma_f32_16x16x32_bf16 v[114:117], v[174:177], v[190:193], v[114:117]
	v_mfma_f32_16x16x32_bf16 v[106:109], v[182:185], v[190:193], v[106:109]
	v_mfma_f32_16x16x32_bf16 v[98:101], v[174:177], v[198:201], v[98:101]
	v_mfma_f32_16x16x32_bf16 v[90:93], v[182:185], v[198:201], v[90:93]
	v_mfma_f32_16x16x32_bf16 v[82:85], v[174:177], v[206:209], v[82:85]
	v_mfma_f32_16x16x32_bf16 v[74:77], v[182:185], v[206:209], v[74:77]
	v_mfma_f32_16x16x32_bf16 v[70:73], v[174:177], v[214:217], v[70:73]
	v_mfma_f32_16x16x32_bf16 v[66:69], v[182:185], v[214:217], v[66:69]
	s_barrier
	s_setprio 0
	s_add_i32 s60, s48, s40
	v_lshl_add_u64 v[146:147], s[34:35], 0, v[132:133]
	s_mov_b32 m0, s60
	ds_read_b128 v[186:189], v152 offset:16384
	ds_read_b128 v[190:193], v152 offset:17408
	ds_read_b128 v[194:197], v152 offset:18432
	ds_read_b128 v[198:201], v152 offset:19456
	ds_read_b128 v[202:205], v152 offset:20480
	ds_read_b128 v[206:209], v152 offset:21504
	ds_read_b128 v[210:213], v152 offset:22528
	ds_read_b128 v[214:217], v152 offset:23552
	global_load_lds_dwordx4 v[146:147], off
	s_add_i32 m0, s60, 0x2000
	s_add_u32 s60, s34, 0x80000
	v_lshl_add_u64 v[218:219], s[34:35], 0, v[136:137]
	s_addc_u32 s61, s35, 0
	s_add_i32 s62, s49, s40
	global_load_lds_dwordx4 v[218:219], off
	v_lshl_add_u64 v[220:221], s[60:61], 0, v[132:133]
	s_mov_b32 m0, s62
	v_lshl_add_u64 v[222:223], s[36:37], 0, v[134:135]
	global_load_lds_dwordx4 v[220:221], off
	v_lshl_add_u64 v[220:221], s[60:61], 0, v[136:137]
	s_add_i32 m0, s62, 0x2000
	s_nop 0
	global_load_lds_dwordx4 v[220:221], off
	v_lshl_add_u64 v[220:221], s[36:37], 0, v[130:131]
	s_mov_b32 m0, s29
	s_nop 0
	global_load_lds_dwordx4 v[220:221], off
	s_mov_b32 m0, s41
	s_nop 0
	global_load_lds_dwordx4 v[222:223], off
	s_waitcnt vmcnt(8)
	s_waitcnt lgkmcnt(0)
	s_setprio 1
	s_barrier
	v_mfma_f32_16x16x32_bf16 v[62:65], v[154:157], v[186:189], v[62:65]
	v_mfma_f32_16x16x32_bf16 v[58:61], v[162:165], v[186:189], v[58:61]
	v_mfma_f32_16x16x32_bf16 v[54:57], v[154:157], v[194:197], v[54:57]
	v_mfma_f32_16x16x32_bf16 v[46:49], v[162:165], v[194:197], v[46:49]
	v_mfma_f32_16x16x32_bf16 v[38:41], v[154:157], v[202:205], v[38:41]
	v_mfma_f32_16x16x32_bf16 v[30:33], v[162:165], v[202:205], v[30:33]
	v_mfma_f32_16x16x32_bf16 v[22:25], v[154:157], v[210:213], v[22:25]
	v_mfma_f32_16x16x32_bf16 v[14:17], v[162:165], v[210:213], v[14:17]
	v_mfma_f32_16x16x32_bf16 v[62:65], v[158:161], v[190:193], v[62:65]
	v_mfma_f32_16x16x32_bf16 v[58:61], v[166:169], v[190:193], v[58:61]
	v_mfma_f32_16x16x32_bf16 v[54:57], v[158:161], v[198:201], v[54:57]
	v_mfma_f32_16x16x32_bf16 v[46:49], v[166:169], v[198:201], v[46:49]
	v_mfma_f32_16x16x32_bf16 v[38:41], v[158:161], v[206:209], v[38:41]
	v_mfma_f32_16x16x32_bf16 v[30:33], v[166:169], v[206:209], v[30:33]
	v_mfma_f32_16x16x32_bf16 v[22:25], v[158:161], v[214:217], v[22:25]
	v_mfma_f32_16x16x32_bf16 v[14:17], v[166:169], v[214:217], v[14:17]
	s_setprio 0
	s_setprio 1
	v_mfma_f32_16x16x32_bf16 v[50:53], v[170:173], v[186:189], v[50:53]
	v_mfma_f32_16x16x32_bf16 v[42:45], v[178:181], v[186:189], v[42:45]
	v_mfma_f32_16x16x32_bf16 v[34:37], v[170:173], v[194:197], v[34:37]
	v_mfma_f32_16x16x32_bf16 v[26:29], v[178:181], v[194:197], v[26:29]
	v_mfma_f32_16x16x32_bf16 v[18:21], v[170:173], v[202:205], v[18:21]
	v_mfma_f32_16x16x32_bf16 v[10:13], v[178:181], v[202:205], v[10:13]
	v_mfma_f32_16x16x32_bf16 v[6:9], v[170:173], v[210:213], v[6:9]
	v_mfma_f32_16x16x32_bf16 v[2:5], v[178:181], v[210:213], v[2:5]
	v_mfma_f32_16x16x32_bf16 v[50:53], v[174:177], v[190:193], v[50:53]
	v_mfma_f32_16x16x32_bf16 v[42:45], v[182:185], v[190:193], v[42:45]
	v_mfma_f32_16x16x32_bf16 v[34:37], v[174:177], v[198:201], v[34:37]
	v_mfma_f32_16x16x32_bf16 v[26:29], v[182:185], v[198:201], v[26:29]
	v_mfma_f32_16x16x32_bf16 v[18:21], v[174:177], v[206:209], v[18:21]
	v_mfma_f32_16x16x32_bf16 v[10:13], v[182:185], v[206:209], v[10:13]
	v_mfma_f32_16x16x32_bf16 v[6:9], v[174:177], v[214:217], v[6:9]
	v_mfma_f32_16x16x32_bf16 v[2:5], v[182:185], v[214:217], v[2:5]
	s_barrier
	s_setprio 0
	s_add_i32 s60, 0, 0x18000
	v_add_u32_e32 v153, s60, v148
	s_add_i32 s61, 0, 0x1c000
	ds_read_b128 v[154:157], v153
	ds_read_b128 v[158:161], v153 offset:1024
	ds_read_b128 v[162:165], v153 offset:2048
	ds_read_b128 v[166:169], v153 offset:3072
	v_add_u32_e32 v153, s61, v148
	ds_read_b128 v[170:173], v153
	ds_read_b128 v[174:177], v153 offset:1024
	ds_read_b128 v[178:181], v153 offset:2048
	ds_read_b128 v[182:185], v153 offset:3072
	s_add_u32 s36, s36, 0x80000
	s_addc_u32 s37, s37, 0
	s_mov_b32 m0, s42
	v_lshl_add_u64 v[224:225], s[36:37], 0, v[130:131]
	ds_read_b128 v[186:189], v152 offset:32768
	ds_read_b128 v[190:193], v152 offset:33792
	ds_read_b128 v[194:197], v152 offset:34816
	ds_read_b128 v[198:201], v152 offset:35840
	ds_read_b128 v[202:205], v152 offset:36864
	ds_read_b128 v[206:209], v152 offset:37888
	ds_read_b128 v[210:213], v152 offset:38912
	ds_read_b128 v[214:217], v152 offset:39936
	global_load_lds_dwordx4 v[224:225], off
	v_lshl_add_u64 v[224:225], s[36:37], 0, v[134:135]
	s_mov_b32 m0, s43
	s_nop 0
	global_load_lds_dwordx4 v[224:225], off
	s_waitcnt vmcnt(8)
	s_waitcnt lgkmcnt(0)
	s_setprio 1
	s_barrier
	v_mfma_f32_16x16x32_bf16 v[126:129], v[154:157], v[186:189], v[126:129]
	v_mfma_f32_16x16x32_bf16 v[122:125], v[162:165], v[186:189], v[122:125]
	v_mfma_f32_16x16x32_bf16 v[118:121], v[154:157], v[194:197], v[118:121]
	v_mfma_f32_16x16x32_bf16 v[110:113], v[162:165], v[194:197], v[110:113]
	v_mfma_f32_16x16x32_bf16 v[102:105], v[154:157], v[202:205], v[102:105]
	v_mfma_f32_16x16x32_bf16 v[94:97], v[162:165], v[202:205], v[94:97]
	v_mfma_f32_16x16x32_bf16 v[86:89], v[154:157], v[210:213], v[86:89]
	v_mfma_f32_16x16x32_bf16 v[78:81], v[162:165], v[210:213], v[78:81]
	v_mfma_f32_16x16x32_bf16 v[126:129], v[158:161], v[190:193], v[126:129]
	v_mfma_f32_16x16x32_bf16 v[122:125], v[166:169], v[190:193], v[122:125]
	v_mfma_f32_16x16x32_bf16 v[118:121], v[158:161], v[198:201], v[118:121]
	v_mfma_f32_16x16x32_bf16 v[110:113], v[166:169], v[198:201], v[110:113]
	v_mfma_f32_16x16x32_bf16 v[102:105], v[158:161], v[206:209], v[102:105]
	v_mfma_f32_16x16x32_bf16 v[94:97], v[166:169], v[206:209], v[94:97]
	v_mfma_f32_16x16x32_bf16 v[86:89], v[158:161], v[214:217], v[86:89]
	v_mfma_f32_16x16x32_bf16 v[78:81], v[166:169], v[214:217], v[78:81]
	s_setprio 0
	s_setprio 1
	v_mfma_f32_16x16x32_bf16 v[114:117], v[170:173], v[186:189], v[114:117]
	v_mfma_f32_16x16x32_bf16 v[106:109], v[178:181], v[186:189], v[106:109]
	v_mfma_f32_16x16x32_bf16 v[98:101], v[170:173], v[194:197], v[98:101]
	v_mfma_f32_16x16x32_bf16 v[90:93], v[178:181], v[194:197], v[90:93]
	v_mfma_f32_16x16x32_bf16 v[82:85], v[170:173], v[202:205], v[82:85]
	v_mfma_f32_16x16x32_bf16 v[74:77], v[178:181], v[202:205], v[74:77]
	v_mfma_f32_16x16x32_bf16 v[70:73], v[170:173], v[210:213], v[70:73]
	v_mfma_f32_16x16x32_bf16 v[66:69], v[178:181], v[210:213], v[66:69]
	v_mfma_f32_16x16x32_bf16 v[114:117], v[174:177], v[190:193], v[114:117]
	v_mfma_f32_16x16x32_bf16 v[106:109], v[182:185], v[190:193], v[106:109]
	v_mfma_f32_16x16x32_bf16 v[98:101], v[174:177], v[198:201], v[98:101]
	v_mfma_f32_16x16x32_bf16 v[90:93], v[182:185], v[198:201], v[90:93]
	v_mfma_f32_16x16x32_bf16 v[82:85], v[174:177], v[206:209], v[82:85]
	v_mfma_f32_16x16x32_bf16 v[74:77], v[182:185], v[206:209], v[74:77]
	v_mfma_f32_16x16x32_bf16 v[70:73], v[174:177], v[214:217], v[70:73]
	v_mfma_f32_16x16x32_bf16 v[66:69], v[182:185], v[214:217], v[66:69]
	s_barrier
	s_setprio 0
	s_add_i32 s36, s60, s40
	v_lshl_add_u64 v[146:147], v[146:147], 0, s[10:11]
	s_mov_b32 m0, s36
	ds_read_b128 v[186:189], v152 offset:49152
	ds_read_b128 v[190:193], v152 offset:50176
	ds_read_b128 v[194:197], v152 offset:51200
	ds_read_b128 v[198:201], v152 offset:52224
	ds_read_b128 v[202:205], v152 offset:53248
	ds_read_b128 v[206:209], v152 offset:54272
	ds_read_b128 v[210:213], v152 offset:55296
	ds_read_b128 v[214:217], v152 offset:56320
	global_load_lds_dwordx4 v[146:147], off
	s_add_i32 m0, s36, 0x2000
	s_add_u32 s34, s34, 0x80080
	v_lshl_add_u64 v[146:147], v[218:219], 0, s[10:11]
	s_addc_u32 s35, s35, 0
	s_add_i32 s36, s61, s40
	global_load_lds_dwordx4 v[146:147], off
	v_lshl_add_u64 v[146:147], s[34:35], 0, v[132:133]
	s_mov_b32 m0, s36
	s_nop 0
	global_load_lds_dwordx4 v[146:147], off
	v_lshl_add_u64 v[146:147], s[34:35], 0, v[136:137]
	s_add_i32 m0, s36, 0x2000
	s_nop 0
	global_load_lds_dwordx4 v[146:147], off
	v_lshl_add_u64 v[146:147], v[220:221], 0, s[10:11]
	s_mov_b32 m0, s45
	s_nop 0
	global_load_lds_dwordx4 v[146:147], off
	v_lshl_add_u64 v[146:147], v[222:223], 0, s[10:11]
	s_mov_b32 m0, s46
	s_nop 0
	global_load_lds_dwordx4 v[146:147], off
	s_waitcnt vmcnt(8)
	s_waitcnt lgkmcnt(0)
	s_setprio 1
	s_barrier
	v_mfma_f32_16x16x32_bf16 v[62:65], v[154:157], v[186:189], v[62:65]
	v_mfma_f32_16x16x32_bf16 v[58:61], v[162:165], v[186:189], v[58:61]
	v_mfma_f32_16x16x32_bf16 v[54:57], v[154:157], v[194:197], v[54:57]
	v_mfma_f32_16x16x32_bf16 v[46:49], v[162:165], v[194:197], v[46:49]
	v_mfma_f32_16x16x32_bf16 v[38:41], v[154:157], v[202:205], v[38:41]
	v_mfma_f32_16x16x32_bf16 v[30:33], v[162:165], v[202:205], v[30:33]
	v_mfma_f32_16x16x32_bf16 v[22:25], v[154:157], v[210:213], v[22:25]
	v_mfma_f32_16x16x32_bf16 v[14:17], v[162:165], v[210:213], v[14:17]
	v_mfma_f32_16x16x32_bf16 v[62:65], v[158:161], v[190:193], v[62:65]
	v_mfma_f32_16x16x32_bf16 v[58:61], v[166:169], v[190:193], v[58:61]
	v_mfma_f32_16x16x32_bf16 v[54:57], v[158:161], v[198:201], v[54:57]
	v_mfma_f32_16x16x32_bf16 v[46:49], v[166:169], v[198:201], v[46:49]
	v_mfma_f32_16x16x32_bf16 v[38:41], v[158:161], v[206:209], v[38:41]
	v_mfma_f32_16x16x32_bf16 v[30:33], v[166:169], v[206:209], v[30:33]
	v_mfma_f32_16x16x32_bf16 v[22:25], v[158:161], v[214:217], v[22:25]
	v_mfma_f32_16x16x32_bf16 v[14:17], v[166:169], v[214:217], v[14:17]
	s_setprio 0
	s_setprio 1
	v_mfma_f32_16x16x32_bf16 v[50:53], v[170:173], v[186:189], v[50:53]
	v_mfma_f32_16x16x32_bf16 v[42:45], v[178:181], v[186:189], v[42:45]
	v_mfma_f32_16x16x32_bf16 v[34:37], v[170:173], v[194:197], v[34:37]
	v_mfma_f32_16x16x32_bf16 v[26:29], v[178:181], v[194:197], v[26:29]
	v_mfma_f32_16x16x32_bf16 v[18:21], v[170:173], v[202:205], v[18:21]
	v_mfma_f32_16x16x32_bf16 v[10:13], v[178:181], v[202:205], v[10:13]
	v_mfma_f32_16x16x32_bf16 v[6:9], v[170:173], v[210:213], v[6:9]
	v_mfma_f32_16x16x32_bf16 v[2:5], v[178:181], v[210:213], v[2:5]
	v_mfma_f32_16x16x32_bf16 v[50:53], v[174:177], v[190:193], v[50:53]
	v_mfma_f32_16x16x32_bf16 v[42:45], v[182:185], v[190:193], v[42:45]
	v_mfma_f32_16x16x32_bf16 v[34:37], v[174:177], v[198:201], v[34:37]
	v_mfma_f32_16x16x32_bf16 v[26:29], v[182:185], v[198:201], v[26:29]
	v_mfma_f32_16x16x32_bf16 v[18:21], v[174:177], v[206:209], v[18:21]
	v_mfma_f32_16x16x32_bf16 v[10:13], v[182:185], v[206:209], v[10:13]
	v_mfma_f32_16x16x32_bf16 v[6:9], v[174:177], v[214:217], v[6:9]
	v_mfma_f32_16x16x32_bf16 v[2:5], v[182:185], v[214:217], v[2:5]
	s_barrier
	s_setprio 0
	s_add_i32 s59, s59, 2
	s_add_u32 s30, s30, 0x100
	s_addc_u32 s31, s31, 0
	s_add_u32 s57, s57, 0x100
	s_addc_u32 s58, s58, 0
	s_cmp_gt_u32 s59, 29
	s_cbranch_scc0 .LBB0_1346
	s_and_b64 vcc, exec, s[12:13]
	s_cbranch_vccz .LBB0_1349
	s_barrier

.LBB0_1479:
	ds_read_b128 v[154:157], v150
	ds_read_b128 v[158:161], v150 offset:1024
	ds_read_b128 v[162:165], v150 offset:2048
	ds_read_b128 v[166:169], v150 offset:3072
	ds_read_b128 v[170:173], v151
	ds_read_b128 v[174:177], v151 offset:1024
	ds_read_b128 v[178:181], v151 offset:2048
	ds_read_b128 v[182:185], v151 offset:3072
	s_add_u32 s30, s28, 0xfff80080
	s_addc_u32 s31, s29, -1
	s_cmp_eq_u32 s54, 28
	s_cselect_b32 s35, s19, s31
	s_cselect_b32 s34, s27, s30
	s_cselect_b32 s31, s17, s53
	s_cselect_b32 s30, s51, s52
	v_lshl_add_u64 v[218:219], s[28:29], 0, v[140:141]
	s_add_i32 m0, s39, 0xc000
	ds_read_b128 v[186:189], v152
	ds_read_b128 v[190:193], v152 offset:1024
	ds_read_b128 v[194:197], v152 offset:2048
	ds_read_b128 v[198:201], v152 offset:3072
	ds_read_b128 v[202:205], v152 offset:4096
	ds_read_b128 v[206:209], v152 offset:5120
	ds_read_b128 v[210:213], v152 offset:6144
	ds_read_b128 v[214:217], v152 offset:7168
	global_load_lds_dwordx4 v[218:219], off
	v_lshl_add_u64 v[218:219], s[28:29], 0, v[142:143]
	s_add_i32 m0, s39, 0xe000
	s_nop 0
	global_load_lds_dwordx4 v[218:219], off
	s_waitcnt vmcnt(8)
	s_waitcnt lgkmcnt(0)
	s_setprio 1
	s_barrier
	v_mfma_f32_16x16x32_bf16 v[126:129], v[154:157], v[186:189], v[126:129]
	v_mfma_f32_16x16x32_bf16 v[122:125], v[162:165], v[186:189], v[122:125]
	v_mfma_f32_16x16x32_bf16 v[118:121], v[154:157], v[194:197], v[118:121]
	v_mfma_f32_16x16x32_bf16 v[114:117], v[162:165], v[194:197], v[114:117]
	v_mfma_f32_16x16x32_bf16 v[110:113], v[154:157], v[202:205], v[110:113]
	v_mfma_f32_16x16x32_bf16 v[102:105], v[162:165], v[202:205], v[102:105]
	v_mfma_f32_16x16x32_bf16 v[94:97], v[154:157], v[210:213], v[94:97]
	v_mfma_f32_16x16x32_bf16 v[86:89], v[162:165], v[210:213], v[86:89]
	v_mfma_f32_16x16x32_bf16 v[126:129], v[158:161], v[190:193], v[126:129]
	v_mfma_f32_16x16x32_bf16 v[122:125], v[166:169], v[190:193], v[122:125]
	v_mfma_f32_16x16x32_bf16 v[118:121], v[158:161], v[198:201], v[118:121]
	v_mfma_f32_16x16x32_bf16 v[114:117], v[166:169], v[198:201], v[114:117]
	v_mfma_f32_16x16x32_bf16 v[110:113], v[158:161], v[206:209], v[110:113]
	v_mfma_f32_16x16x32_bf16 v[102:105], v[166:169], v[206:209], v[102:105]
	v_mfma_f32_16x16x32_bf16 v[94:97], v[158:161], v[214:217], v[94:97]
	v_mfma_f32_16x16x32_bf16 v[86:89], v[166:169], v[214:217], v[86:89]
	s_setprio 0
	s_setprio 1
	v_mfma_f32_16x16x32_bf16 v[106:109], v[170:173], v[186:189], v[106:109]
	v_mfma_f32_16x16x32_bf16 v[98:101], v[178:181], v[186:189], v[98:101]
	v_mfma_f32_16x16x32_bf16 v[90:93], v[170:173], v[194:197], v[90:93]
	v_mfma_f32_16x16x32_bf16 v[82:85], v[178:181], v[194:197], v[82:85]
	v_mfma_f32_16x16x32_bf16 v[78:81], v[170:173], v[202:205], v[78:81]
	v_mfma_f32_16x16x32_bf16 v[74:77], v[178:181], v[202:205], v[74:77]
	v_mfma_f32_16x16x32_bf16 v[70:73], v[170:173], v[210:213], v[70:73]
	v_mfma_f32_16x16x32_bf16 v[66:69], v[178:181], v[210:213], v[66:69]
	v_mfma_f32_16x16x32_bf16 v[106:109], v[174:177], v[190:193], v[106:109]
	v_mfma_f32_16x16x32_bf16 v[98:101], v[182:185], v[190:193], v[98:101]
	v_mfma_f32_16x16x32_bf16 v[90:93], v[174:177], v[198:201], v[90:93]
	v_mfma_f32_16x16x32_bf16 v[82:85], v[182:185], v[198:201], v[82:85]
	v_mfma_f32_16x16x32_bf16 v[78:81], v[174:177], v[206:209], v[78:81]
	v_mfma_f32_16x16x32_bf16 v[74:77], v[182:185], v[206:209], v[74:77]
	v_mfma_f32_16x16x32_bf16 v[70:73], v[174:177], v[214:217], v[70:73]
	v_mfma_f32_16x16x32_bf16 v[66:69], v[182:185], v[214:217], v[66:69]
	s_barrier
	s_setprio 0
	s_add_i32 s55, s47, s36
	v_lshl_add_u64 v[218:219], s[30:31], 0, v[134:135]
	s_mov_b32 m0, s55
	ds_read_b128 v[186:189], v152 offset:16384
	ds_read_b128 v[190:193], v152 offset:17408
	ds_read_b128 v[194:197], v152 offset:18432
	ds_read_b128 v[198:201], v152 offset:19456
	ds_read_b128 v[202:205], v152 offset:20480
	ds_read_b128 v[206:209], v152 offset:21504
	ds_read_b128 v[210:213], v152 offset:22528
	ds_read_b128 v[214:217], v152 offset:23552
	global_load_lds_dwordx4 v[218:219], off
	s_add_i32 m0, s55, 0x2000
	s_add_u32 s56, s30, 0x80000
	v_lshl_add_u64 v[220:221], s[30:31], 0, v[130:131]
	s_addc_u32 s57, s31, 0
	s_add_i32 s55, s48, s36
	global_load_lds_dwordx4 v[220:221], off
	v_lshl_add_u64 v[222:223], s[56:57], 0, v[134:135]
	s_mov_b32 m0, s55
	v_lshl_add_u64 v[224:225], s[34:35], 0, v[132:133]
	global_load_lds_dwordx4 v[222:223], off
	v_lshl_add_u64 v[222:223], s[56:57], 0, v[130:131]
	s_add_i32 m0, s55, 0x2000
	s_nop 0
	global_load_lds_dwordx4 v[222:223], off
	v_lshl_add_u64 v[222:223], s[34:35], 0, v[136:137]
	s_mov_b32 m0, s39
	s_nop 0
	global_load_lds_dwordx4 v[222:223], off
	s_mov_b32 m0, s40
	s_nop 0
	global_load_lds_dwordx4 v[224:225], off
	s_waitcnt vmcnt(8)
	s_waitcnt lgkmcnt(0)
	s_setprio 1
	s_barrier
	v_mfma_f32_16x16x32_bf16 v[62:65], v[154:157], v[186:189], v[62:65]
	v_mfma_f32_16x16x32_bf16 v[58:61], v[162:165], v[186:189], v[58:61]
	v_mfma_f32_16x16x32_bf16 v[54:57], v[154:157], v[194:197], v[54:57]
	v_mfma_f32_16x16x32_bf16 v[50:53], v[162:165], v[194:197], v[50:53]
	v_mfma_f32_16x16x32_bf16 v[46:49], v[154:157], v[202:205], v[46:49]
	v_mfma_f32_16x16x32_bf16 v[38:41], v[162:165], v[202:205], v[38:41]
	v_mfma_f32_16x16x32_bf16 v[30:33], v[154:157], v[210:213], v[30:33]
	v_mfma_f32_16x16x32_bf16 v[22:25], v[162:165], v[210:213], v[22:25]
	v_mfma_f32_16x16x32_bf16 v[62:65], v[158:161], v[190:193], v[62:65]
	v_mfma_f32_16x16x32_bf16 v[58:61], v[166:169], v[190:193], v[58:61]
	v_mfma_f32_16x16x32_bf16 v[54:57], v[158:161], v[198:201], v[54:57]
	v_mfma_f32_16x16x32_bf16 v[50:53], v[166:169], v[198:201], v[50:53]
	v_mfma_f32_16x16x32_bf16 v[46:49], v[158:161], v[206:209], v[46:49]
	v_mfma_f32_16x16x32_bf16 v[38:41], v[166:169], v[206:209], v[38:41]
	v_mfma_f32_16x16x32_bf16 v[30:33], v[158:161], v[214:217], v[30:33]
	v_mfma_f32_16x16x32_bf16 v[22:25], v[166:169], v[214:217], v[22:25]
	s_setprio 0
	s_setprio 1
	v_mfma_f32_16x16x32_bf16 v[42:45], v[170:173], v[186:189], v[42:45]
	v_mfma_f32_16x16x32_bf16 v[34:37], v[178:181], v[186:189], v[34:37]
	v_mfma_f32_16x16x32_bf16 v[26:29], v[170:173], v[194:197], v[26:29]
	v_mfma_f32_16x16x32_bf16 v[18:21], v[178:181], v[194:197], v[18:21]
	v_mfma_f32_16x16x32_bf16 v[14:17], v[170:173], v[202:205], v[14:17]
	v_mfma_f32_16x16x32_bf16 v[10:13], v[178:181], v[202:205], v[10:13]
	v_mfma_f32_16x16x32_bf16 v[6:9], v[170:173], v[210:213], v[6:9]
	v_mfma_f32_16x16x32_bf16 v[2:5], v[178:181], v[210:213], v[2:5]
	v_mfma_f32_16x16x32_bf16 v[42:45], v[174:177], v[190:193], v[42:45]
	v_mfma_f32_16x16x32_bf16 v[34:37], v[182:185], v[190:193], v[34:37]
	v_mfma_f32_16x16x32_bf16 v[26:29], v[174:177], v[198:201], v[26:29]
	v_mfma_f32_16x16x32_bf16 v[18:21], v[182:185], v[198:201], v[18:21]
	v_mfma_f32_16x16x32_bf16 v[14:17], v[174:177], v[206:209], v[14:17]
	v_mfma_f32_16x16x32_bf16 v[10:13], v[182:185], v[206:209], v[10:13]
	v_mfma_f32_16x16x32_bf16 v[6:9], v[174:177], v[214:217], v[6:9]
	v_mfma_f32_16x16x32_bf16 v[2:5], v[182:185], v[214:217], v[2:5]
	s_barrier
	s_setprio 0
	s_add_i32 s55, 0, 0x18000
	v_add_u32_e32 v153, s55, v148
	s_add_i32 s56, 0, 0x1c000
	ds_read_b128 v[154:157], v153
	ds_read_b128 v[158:161], v153 offset:1024
	ds_read_b128 v[162:165], v153 offset:2048
	ds_read_b128 v[166:169], v153 offset:3072
	v_add_u32_e32 v153, s56, v148
	ds_read_b128 v[170:173], v153
	ds_read_b128 v[174:177], v153 offset:1024
	ds_read_b128 v[178:181], v153 offset:2048
	ds_read_b128 v[182:185], v153 offset:3072
	s_add_u32 s34, s34, 0x80000
	s_addc_u32 s35, s35, 0
	s_mov_b32 m0, s41
	v_lshl_add_u64 v[226:227], s[34:35], 0, v[136:137]
	ds_read_b128 v[186:189], v152 offset:32768
	ds_read_b128 v[190:193], v152 offset:33792
	ds_read_b128 v[194:197], v152 offset:34816
	ds_read_b128 v[198:201], v152 offset:35840
	ds_read_b128 v[202:205], v152 offset:36864
	ds_read_b128 v[206:209], v152 offset:37888
	ds_read_b128 v[210:213], v152 offset:38912
	ds_read_b128 v[214:217], v152 offset:39936
	global_load_lds_dwordx4 v[226:227], off
	v_lshl_add_u64 v[226:227], s[34:35], 0, v[132:133]
	s_mov_b32 m0, s42
	s_nop 0
	global_load_lds_dwordx4 v[226:227], off
	s_waitcnt vmcnt(8)
	s_waitcnt lgkmcnt(0)
	s_setprio 1
	s_barrier
	v_mfma_f32_16x16x32_bf16 v[126:129], v[154:157], v[186:189], v[126:129]
	v_mfma_f32_16x16x32_bf16 v[122:125], v[162:165], v[186:189], v[122:125]
	v_mfma_f32_16x16x32_bf16 v[118:121], v[154:157], v[194:197], v[118:121]
	v_mfma_f32_16x16x32_bf16 v[114:117], v[162:165], v[194:197], v[114:117]
	v_mfma_f32_16x16x32_bf16 v[110:113], v[154:157], v[202:205], v[110:113]
	v_mfma_f32_16x16x32_bf16 v[102:105], v[162:165], v[202:205], v[102:105]
	v_mfma_f32_16x16x32_bf16 v[94:97], v[154:157], v[210:213], v[94:97]
	v_mfma_f32_16x16x32_bf16 v[86:89], v[162:165], v[210:213], v[86:89]
	v_mfma_f32_16x16x32_bf16 v[126:129], v[158:161], v[190:193], v[126:129]
	v_mfma_f32_16x16x32_bf16 v[122:125], v[166:169], v[190:193], v[122:125]
	v_mfma_f32_16x16x32_bf16 v[118:121], v[158:161], v[198:201], v[118:121]
	v_mfma_f32_16x16x32_bf16 v[114:117], v[166:169], v[198:201], v[114:117]
	v_mfma_f32_16x16x32_bf16 v[110:113], v[158:161], v[206:209], v[110:113]
	v_mfma_f32_16x16x32_bf16 v[102:105], v[166:169], v[206:209], v[102:105]
	v_mfma_f32_16x16x32_bf16 v[94:97], v[158:161], v[214:217], v[94:97]
	v_mfma_f32_16x16x32_bf16 v[86:89], v[166:169], v[214:217], v[86:89]
	s_setprio 0
	s_setprio 1
	v_mfma_f32_16x16x32_bf16 v[106:109], v[170:173], v[186:189], v[106:109]
	v_mfma_f32_16x16x32_bf16 v[98:101], v[178:181], v[186:189], v[98:101]
	v_mfma_f32_16x16x32_bf16 v[90:93], v[170:173], v[194:197], v[90:93]
	v_mfma_f32_16x16x32_bf16 v[82:85], v[178:181], v[194:197], v[82:85]
	v_mfma_f32_16x16x32_bf16 v[78:81], v[170:173], v[202:205], v[78:81]
	v_mfma_f32_16x16x32_bf16 v[74:77], v[178:181], v[202:205], v[74:77]
	v_mfma_f32_16x16x32_bf16 v[70:73], v[170:173], v[210:213], v[70:73]
	v_mfma_f32_16x16x32_bf16 v[66:69], v[178:181], v[210:213], v[66:69]
	v_mfma_f32_16x16x32_bf16 v[106:109], v[174:177], v[190:193], v[106:109]
	v_mfma_f32_16x16x32_bf16 v[98:101], v[182:185], v[190:193], v[98:101]
	v_mfma_f32_16x16x32_bf16 v[90:93], v[174:177], v[198:201], v[90:93]
	v_mfma_f32_16x16x32_bf16 v[82:85], v[182:185], v[198:201], v[82:85]
	v_mfma_f32_16x16x32_bf16 v[78:81], v[174:177], v[206:209], v[78:81]
	v_mfma_f32_16x16x32_bf16 v[74:77], v[182:185], v[206:209], v[74:77]
	v_mfma_f32_16x16x32_bf16 v[70:73], v[174:177], v[214:217], v[70:73]
	v_mfma_f32_16x16x32_bf16 v[66:69], v[182:185], v[214:217], v[66:69]
	s_barrier
	s_setprio 0
	s_add_i32 s34, s55, s36
	v_lshl_add_u64 v[218:219], v[218:219], 0, s[10:11]
	s_mov_b32 m0, s34
	ds_read_b128 v[186:189], v152 offset:49152
	ds_read_b128 v[190:193], v152 offset:50176
	ds_read_b128 v[194:197], v152 offset:51200
	ds_read_b128 v[198:201], v152 offset:52224
	ds_read_b128 v[202:205], v152 offset:53248
	ds_read_b128 v[206:209], v152 offset:54272
	ds_read_b128 v[210:213], v152 offset:55296
	ds_read_b128 v[214:217], v152 offset:56320
	global_load_lds_dwordx4 v[218:219], off
	s_add_i32 m0, s34, 0x2000
	s_add_u32 s30, s30, 0x80080
	v_lshl_add_u64 v[218:219], v[220:221], 0, s[10:11]
	s_addc_u32 s31, s31, 0
	s_add_i32 s34, s56, s36
	global_load_lds_dwordx4 v[218:219], off
	v_lshl_add_u64 v[218:219], s[30:31], 0, v[134:135]
	s_mov_b32 m0, s34
	s_nop 0
	global_load_lds_dwordx4 v[218:219], off
	v_lshl_add_u64 v[218:219], s[30:31], 0, v[130:131]
	s_add_i32 m0, s34, 0x2000
	s_nop 0
	global_load_lds_dwordx4 v[218:219], off
	v_lshl_add_u64 v[218:219], v[222:223], 0, s[10:11]
	s_mov_b32 m0, s44
	s_nop 0
	global_load_lds_dwordx4 v[218:219], off
	v_lshl_add_u64 v[218:219], v[224:225], 0, s[10:11]
	s_mov_b32 m0, s45
	s_nop 0
	global_load_lds_dwordx4 v[218:219], off
	s_waitcnt vmcnt(8)
	s_waitcnt lgkmcnt(0)
	s_setprio 1
	s_barrier
	v_mfma_f32_16x16x32_bf16 v[62:65], v[154:157], v[186:189], v[62:65]
	v_mfma_f32_16x16x32_bf16 v[58:61], v[162:165], v[186:189], v[58:61]
	v_mfma_f32_16x16x32_bf16 v[54:57], v[154:157], v[194:197], v[54:57]
	v_mfma_f32_16x16x32_bf16 v[50:53], v[162:165], v[194:197], v[50:53]
	v_mfma_f32_16x16x32_bf16 v[46:49], v[154:157], v[202:205], v[46:49]
	v_mfma_f32_16x16x32_bf16 v[38:41], v[162:165], v[202:205], v[38:41]
	v_mfma_f32_16x16x32_bf16 v[30:33], v[154:157], v[210:213], v[30:33]
	v_mfma_f32_16x16x32_bf16 v[22:25], v[162:165], v[210:213], v[22:25]
	v_mfma_f32_16x16x32_bf16 v[62:65], v[158:161], v[190:193], v[62:65]
	v_mfma_f32_16x16x32_bf16 v[58:61], v[166:169], v[190:193], v[58:61]
	v_mfma_f32_16x16x32_bf16 v[54:57], v[158:161], v[198:201], v[54:57]
	v_mfma_f32_16x16x32_bf16 v[50:53], v[166:169], v[198:201], v[50:53]
	v_mfma_f32_16x16x32_bf16 v[46:49], v[158:161], v[206:209], v[46:49]
	v_mfma_f32_16x16x32_bf16 v[38:41], v[166:169], v[206:209], v[38:41]
	v_mfma_f32_16x16x32_bf16 v[30:33], v[158:161], v[214:217], v[30:33]
	v_mfma_f32_16x16x32_bf16 v[22:25], v[166:169], v[214:217], v[22:25]
	s_setprio 0
	s_setprio 1
	v_mfma_f32_16x16x32_bf16 v[42:45], v[170:173], v[186:189], v[42:45]
	v_mfma_f32_16x16x32_bf16 v[34:37], v[178:181], v[186:189], v[34:37]
	v_mfma_f32_16x16x32_bf16 v[26:29], v[170:173], v[194:197], v[26:29]
	v_mfma_f32_16x16x32_bf16 v[18:21], v[178:181], v[194:197], v[18:21]
	v_mfma_f32_16x16x32_bf16 v[14:17], v[170:173], v[202:205], v[14:17]
	v_mfma_f32_16x16x32_bf16 v[10:13], v[178:181], v[202:205], v[10:13]
	v_mfma_f32_16x16x32_bf16 v[6:9], v[170:173], v[210:213], v[6:9]
	v_mfma_f32_16x16x32_bf16 v[2:5], v[178:181], v[210:213], v[2:5]
	v_mfma_f32_16x16x32_bf16 v[42:45], v[174:177], v[190:193], v[42:45]
	v_mfma_f32_16x16x32_bf16 v[34:37], v[182:185], v[190:193], v[34:37]
	v_mfma_f32_16x16x32_bf16 v[26:29], v[174:177], v[198:201], v[26:29]
	v_mfma_f32_16x16x32_bf16 v[18:21], v[182:185], v[198:201], v[18:21]
	v_mfma_f32_16x16x32_bf16 v[14:17], v[174:177], v[206:209], v[14:17]
	v_mfma_f32_16x16x32_bf16 v[10:13], v[182:185], v[206:209], v[10:13]
	v_mfma_f32_16x16x32_bf16 v[6:9], v[174:177], v[214:217], v[6:9]
	v_mfma_f32_16x16x32_bf16 v[2:5], v[182:185], v[214:217], v[2:5]
	s_barrier
	s_setprio 0
	s_add_i32 s54, s54, 2
	s_add_u32 s28, s28, 0x100
	s_addc_u32 s29, s29, 0
	s_add_u32 s52, s52, 0x100
	s_addc_u32 s53, s53, 0
	s_cmp_gt_u32 s54, 29
	s_cbranch_scc0 .LBB0_1479
	s_and_b64 vcc, exec, s[12:13]
	s_cbranch_vccz .LBB0_1482
	s_barrier

.LBB0_1562:
	ds_read_b128 v[154:157], v150
	ds_read_b128 v[158:161], v150 offset:1024
	ds_read_b128 v[162:165], v150 offset:2048
	ds_read_b128 v[166:169], v150 offset:3072
	ds_read_b128 v[170:173], v151
	ds_read_b128 v[174:177], v151 offset:1024
	ds_read_b128 v[178:181], v151 offset:2048
	ds_read_b128 v[182:185], v151 offset:3072
	s_add_u32 s28, s26, 0xffea0080
	s_addc_u32 s29, s27, -1
	s_cmpk_eq_i32 s59, 0x54
	s_cselect_b32 s31, s1, s29
	s_cselect_b32 s30, s0, s28
	s_cselect_b32 s29, s25, s58
	s_cselect_b32 s28, s24, s57
	v_lshl_add_u64 v[146:147], s[26:27], 0, v[138:139]
	s_add_i32 m0, s39, 0xc000
	ds_read_b128 v[186:189], v152
	ds_read_b128 v[190:193], v152 offset:1024
	ds_read_b128 v[194:197], v152 offset:2048
	ds_read_b128 v[198:201], v152 offset:3072
	ds_read_b128 v[202:205], v152 offset:4096
	ds_read_b128 v[206:209], v152 offset:5120
	ds_read_b128 v[210:213], v152 offset:6144
	ds_read_b128 v[214:217], v152 offset:7168
	global_load_lds_dwordx4 v[146:147], off
	v_lshl_add_u64 v[146:147], s[26:27], 0, v[140:141]
	s_add_i32 m0, s39, 0xe000
	s_nop 0
	global_load_lds_dwordx4 v[146:147], off
	s_waitcnt vmcnt(8)
	s_waitcnt lgkmcnt(0)
	s_setprio 1
	s_barrier
	v_mfma_f32_16x16x32_bf16 v[126:129], v[154:157], v[186:189], v[126:129]
	v_mfma_f32_16x16x32_bf16 v[122:125], v[162:165], v[186:189], v[122:125]
	v_mfma_f32_16x16x32_bf16 v[118:121], v[154:157], v[194:197], v[118:121]
	v_mfma_f32_16x16x32_bf16 v[110:113], v[162:165], v[194:197], v[110:113]
	v_mfma_f32_16x16x32_bf16 v[102:105], v[154:157], v[202:205], v[102:105]
	v_mfma_f32_16x16x32_bf16 v[94:97], v[162:165], v[202:205], v[94:97]
	v_mfma_f32_16x16x32_bf16 v[86:89], v[154:157], v[210:213], v[86:89]
	v_mfma_f32_16x16x32_bf16 v[78:81], v[162:165], v[210:213], v[78:81]
	v_mfma_f32_16x16x32_bf16 v[126:129], v[158:161], v[190:193], v[126:129]
	v_mfma_f32_16x16x32_bf16 v[122:125], v[166:169], v[190:193], v[122:125]
	v_mfma_f32_16x16x32_bf16 v[118:121], v[158:161], v[198:201], v[118:121]
	v_mfma_f32_16x16x32_bf16 v[110:113], v[166:169], v[198:201], v[110:113]
	v_mfma_f32_16x16x32_bf16 v[102:105], v[158:161], v[206:209], v[102:105]
	v_mfma_f32_16x16x32_bf16 v[94:97], v[166:169], v[206:209], v[94:97]
	v_mfma_f32_16x16x32_bf16 v[86:89], v[158:161], v[214:217], v[86:89]
	v_mfma_f32_16x16x32_bf16 v[78:81], v[166:169], v[214:217], v[78:81]
	s_setprio 0
	s_setprio 1
	v_mfma_f32_16x16x32_bf16 v[114:117], v[170:173], v[186:189], v[114:117]
	v_mfma_f32_16x16x32_bf16 v[106:109], v[178:181], v[186:189], v[106:109]
	v_mfma_f32_16x16x32_bf16 v[98:101], v[170:173], v[194:197], v[98:101]
	v_mfma_f32_16x16x32_bf16 v[90:93], v[178:181], v[194:197], v[90:93]
	v_mfma_f32_16x16x32_bf16 v[82:85], v[170:173], v[202:205], v[82:85]
	v_mfma_f32_16x16x32_bf16 v[74:77], v[178:181], v[202:205], v[74:77]
	v_mfma_f32_16x16x32_bf16 v[70:73], v[170:173], v[210:213], v[70:73]
	v_mfma_f32_16x16x32_bf16 v[66:69], v[178:181], v[210:213], v[66:69]
	v_mfma_f32_16x16x32_bf16 v[114:117], v[174:177], v[190:193], v[114:117]
	v_mfma_f32_16x16x32_bf16 v[106:109], v[182:185], v[190:193], v[106:109]
	v_mfma_f32_16x16x32_bf16 v[98:101], v[174:177], v[198:201], v[98:101]
	v_mfma_f32_16x16x32_bf16 v[90:93], v[182:185], v[198:201], v[90:93]
	v_mfma_f32_16x16x32_bf16 v[82:85], v[174:177], v[206:209], v[82:85]
	v_mfma_f32_16x16x32_bf16 v[74:77], v[182:185], v[206:209], v[74:77]
	v_mfma_f32_16x16x32_bf16 v[70:73], v[174:177], v[214:217], v[70:73]
	v_mfma_f32_16x16x32_bf16 v[66:69], v[182:185], v[214:217], v[66:69]
	s_barrier
	s_setprio 0
	s_add_i32 s60, s47, s38
	v_lshl_add_u64 v[146:147], s[28:29], 0, v[132:133]
	s_mov_b32 m0, s60
	ds_read_b128 v[186:189], v152 offset:16384
	ds_read_b128 v[190:193], v152 offset:17408
	ds_read_b128 v[194:197], v152 offset:18432
	ds_read_b128 v[198:201], v152 offset:19456
	ds_read_b128 v[202:205], v152 offset:20480
	ds_read_b128 v[206:209], v152 offset:21504
	ds_read_b128 v[210:213], v152 offset:22528
	ds_read_b128 v[214:217], v152 offset:23552
	global_load_lds_dwordx4 v[146:147], off
	s_add_i32 m0, s60, 0x2000
	s_add_u32 s60, s28, 0x160000
	v_lshl_add_u64 v[218:219], s[28:29], 0, v[136:137]
	s_addc_u32 s61, s29, 0
	s_add_i32 s62, s48, s38
	global_load_lds_dwordx4 v[218:219], off
	v_lshl_add_u64 v[220:221], s[60:61], 0, v[132:133]
	s_mov_b32 m0, s62
	v_lshl_add_u64 v[222:223], s[30:31], 0, v[134:135]
	global_load_lds_dwordx4 v[220:221], off
	v_lshl_add_u64 v[220:221], s[60:61], 0, v[136:137]
	s_add_i32 m0, s62, 0x2000
	s_nop 0
	global_load_lds_dwordx4 v[220:221], off
	v_lshl_add_u64 v[220:221], s[30:31], 0, v[130:131]
	s_mov_b32 m0, s39
	s_nop 0
	global_load_lds_dwordx4 v[220:221], off
	s_mov_b32 m0, s40
	s_nop 0
	global_load_lds_dwordx4 v[222:223], off
	s_waitcnt vmcnt(8)
	s_waitcnt lgkmcnt(0)
	s_setprio 1
	s_barrier
	v_mfma_f32_16x16x32_bf16 v[62:65], v[154:157], v[186:189], v[62:65]
	v_mfma_f32_16x16x32_bf16 v[58:61], v[162:165], v[186:189], v[58:61]
	v_mfma_f32_16x16x32_bf16 v[54:57], v[154:157], v[194:197], v[54:57]
	v_mfma_f32_16x16x32_bf16 v[46:49], v[162:165], v[194:197], v[46:49]
	v_mfma_f32_16x16x32_bf16 v[38:41], v[154:157], v[202:205], v[38:41]
	v_mfma_f32_16x16x32_bf16 v[30:33], v[162:165], v[202:205], v[30:33]
	v_mfma_f32_16x16x32_bf16 v[22:25], v[154:157], v[210:213], v[22:25]
	v_mfma_f32_16x16x32_bf16 v[14:17], v[162:165], v[210:213], v[14:17]
	v_mfma_f32_16x16x32_bf16 v[62:65], v[158:161], v[190:193], v[62:65]
	v_mfma_f32_16x16x32_bf16 v[58:61], v[166:169], v[190:193], v[58:61]
	v_mfma_f32_16x16x32_bf16 v[54:57], v[158:161], v[198:201], v[54:57]
	v_mfma_f32_16x16x32_bf16 v[46:49], v[166:169], v[198:201], v[46:49]
	v_mfma_f32_16x16x32_bf16 v[38:41], v[158:161], v[206:209], v[38:41]
	v_mfma_f32_16x16x32_bf16 v[30:33], v[166:169], v[206:209], v[30:33]
	v_mfma_f32_16x16x32_bf16 v[22:25], v[158:161], v[214:217], v[22:25]
	v_mfma_f32_16x16x32_bf16 v[14:17], v[166:169], v[214:217], v[14:17]
	s_setprio 0
	s_setprio 1
	v_mfma_f32_16x16x32_bf16 v[50:53], v[170:173], v[186:189], v[50:53]
	v_mfma_f32_16x16x32_bf16 v[42:45], v[178:181], v[186:189], v[42:45]
	v_mfma_f32_16x16x32_bf16 v[34:37], v[170:173], v[194:197], v[34:37]
	v_mfma_f32_16x16x32_bf16 v[26:29], v[178:181], v[194:197], v[26:29]
	v_mfma_f32_16x16x32_bf16 v[18:21], v[170:173], v[202:205], v[18:21]
	v_mfma_f32_16x16x32_bf16 v[10:13], v[178:181], v[202:205], v[10:13]
	v_mfma_f32_16x16x32_bf16 v[6:9], v[170:173], v[210:213], v[6:9]
	v_mfma_f32_16x16x32_bf16 v[2:5], v[178:181], v[210:213], v[2:5]
	v_mfma_f32_16x16x32_bf16 v[50:53], v[174:177], v[190:193], v[50:53]
	v_mfma_f32_16x16x32_bf16 v[42:45], v[182:185], v[190:193], v[42:45]
	v_mfma_f32_16x16x32_bf16 v[34:37], v[174:177], v[198:201], v[34:37]
	v_mfma_f32_16x16x32_bf16 v[26:29], v[182:185], v[198:201], v[26:29]
	v_mfma_f32_16x16x32_bf16 v[18:21], v[174:177], v[206:209], v[18:21]
	v_mfma_f32_16x16x32_bf16 v[10:13], v[182:185], v[206:209], v[10:13]
	v_mfma_f32_16x16x32_bf16 v[6:9], v[174:177], v[214:217], v[6:9]
	v_mfma_f32_16x16x32_bf16 v[2:5], v[182:185], v[214:217], v[2:5]
	s_barrier
	s_setprio 0
	s_add_i32 s60, 0, 0x18000
	v_add_u32_e32 v153, s60, v148
	s_add_i32 s61, 0, 0x1c000
	ds_read_b128 v[154:157], v153
	ds_read_b128 v[158:161], v153 offset:1024
	ds_read_b128 v[162:165], v153 offset:2048
	ds_read_b128 v[166:169], v153 offset:3072
	v_add_u32_e32 v153, s61, v148
	ds_read_b128 v[170:173], v153
	ds_read_b128 v[174:177], v153 offset:1024
	ds_read_b128 v[178:181], v153 offset:2048
	ds_read_b128 v[182:185], v153 offset:3072
	s_add_u32 s30, s30, 0x160000
	s_addc_u32 s31, s31, 0
	s_mov_b32 m0, s41
	v_lshl_add_u64 v[224:225], s[30:31], 0, v[130:131]
	ds_read_b128 v[186:189], v152 offset:32768
	ds_read_b128 v[190:193], v152 offset:33792
	ds_read_b128 v[194:197], v152 offset:34816
	ds_read_b128 v[198:201], v152 offset:35840
	ds_read_b128 v[202:205], v152 offset:36864
	ds_read_b128 v[206:209], v152 offset:37888
	ds_read_b128 v[210:213], v152 offset:38912
	ds_read_b128 v[214:217], v152 offset:39936
	global_load_lds_dwordx4 v[224:225], off
	v_lshl_add_u64 v[224:225], s[30:31], 0, v[134:135]
	s_mov_b32 m0, s42
	s_nop 0
	global_load_lds_dwordx4 v[224:225], off
	s_waitcnt vmcnt(8)
	s_waitcnt lgkmcnt(0)
	s_setprio 1
	s_barrier
	v_mfma_f32_16x16x32_bf16 v[126:129], v[154:157], v[186:189], v[126:129]
	v_mfma_f32_16x16x32_bf16 v[122:125], v[162:165], v[186:189], v[122:125]
	v_mfma_f32_16x16x32_bf16 v[118:121], v[154:157], v[194:197], v[118:121]
	v_mfma_f32_16x16x32_bf16 v[110:113], v[162:165], v[194:197], v[110:113]
	v_mfma_f32_16x16x32_bf16 v[102:105], v[154:157], v[202:205], v[102:105]
	v_mfma_f32_16x16x32_bf16 v[94:97], v[162:165], v[202:205], v[94:97]
	v_mfma_f32_16x16x32_bf16 v[86:89], v[154:157], v[210:213], v[86:89]
	v_mfma_f32_16x16x32_bf16 v[78:81], v[162:165], v[210:213], v[78:81]
	v_mfma_f32_16x16x32_bf16 v[126:129], v[158:161], v[190:193], v[126:129]
	v_mfma_f32_16x16x32_bf16 v[122:125], v[166:169], v[190:193], v[122:125]
	v_mfma_f32_16x16x32_bf16 v[118:121], v[158:161], v[198:201], v[118:121]
	v_mfma_f32_16x16x32_bf16 v[110:113], v[166:169], v[198:201], v[110:113]
	v_mfma_f32_16x16x32_bf16 v[102:105], v[158:161], v[206:209], v[102:105]
	v_mfma_f32_16x16x32_bf16 v[94:97], v[166:169], v[206:209], v[94:97]
	v_mfma_f32_16x16x32_bf16 v[86:89], v[158:161], v[214:217], v[86:89]
	v_mfma_f32_16x16x32_bf16 v[78:81], v[166:169], v[214:217], v[78:81]
	s_setprio 0
	s_setprio 1
	v_mfma_f32_16x16x32_bf16 v[114:117], v[170:173], v[186:189], v[114:117]
	v_mfma_f32_16x16x32_bf16 v[106:109], v[178:181], v[186:189], v[106:109]
	v_mfma_f32_16x16x32_bf16 v[98:101], v[170:173], v[194:197], v[98:101]
	v_mfma_f32_16x16x32_bf16 v[90:93], v[178:181], v[194:197], v[90:93]
	v_mfma_f32_16x16x32_bf16 v[82:85], v[170:173], v[202:205], v[82:85]
	v_mfma_f32_16x16x32_bf16 v[74:77], v[178:181], v[202:205], v[74:77]
	v_mfma_f32_16x16x32_bf16 v[70:73], v[170:173], v[210:213], v[70:73]
	v_mfma_f32_16x16x32_bf16 v[66:69], v[178:181], v[210:213], v[66:69]
	v_mfma_f32_16x16x32_bf16 v[114:117], v[174:177], v[190:193], v[114:117]
	v_mfma_f32_16x16x32_bf16 v[106:109], v[182:185], v[190:193], v[106:109]
	v_mfma_f32_16x16x32_bf16 v[98:101], v[174:177], v[198:201], v[98:101]
	v_mfma_f32_16x16x32_bf16 v[90:93], v[182:185], v[198:201], v[90:93]
	v_mfma_f32_16x16x32_bf16 v[82:85], v[174:177], v[206:209], v[82:85]
	v_mfma_f32_16x16x32_bf16 v[74:77], v[182:185], v[206:209], v[74:77]
	v_mfma_f32_16x16x32_bf16 v[70:73], v[174:177], v[214:217], v[70:73]
	v_mfma_f32_16x16x32_bf16 v[66:69], v[182:185], v[214:217], v[66:69]
	s_barrier
	s_setprio 0
	s_add_i32 s30, s60, s38
	v_lshl_add_u64 v[146:147], v[146:147], 0, s[10:11]
	s_mov_b32 m0, s30
	ds_read_b128 v[186:189], v152 offset:49152
	ds_read_b128 v[190:193], v152 offset:50176
	ds_read_b128 v[194:197], v152 offset:51200
	ds_read_b128 v[198:201], v152 offset:52224
	ds_read_b128 v[202:205], v152 offset:53248
	ds_read_b128 v[206:209], v152 offset:54272
	ds_read_b128 v[210:213], v152 offset:55296
	ds_read_b128 v[214:217], v152 offset:56320
	global_load_lds_dwordx4 v[146:147], off
	s_add_i32 m0, s30, 0x2000
	s_add_u32 s28, s28, 0x160080
	v_lshl_add_u64 v[146:147], v[218:219], 0, s[10:11]
	s_addc_u32 s29, s29, 0
	s_add_i32 s30, s61, s38
	global_load_lds_dwordx4 v[146:147], off
	v_lshl_add_u64 v[146:147], s[28:29], 0, v[132:133]
	s_mov_b32 m0, s30
	s_nop 0
	global_load_lds_dwordx4 v[146:147], off
	v_lshl_add_u64 v[146:147], s[28:29], 0, v[136:137]
	s_add_i32 m0, s30, 0x2000
	s_nop 0
	global_load_lds_dwordx4 v[146:147], off
	v_lshl_add_u64 v[146:147], v[220:221], 0, s[10:11]
	s_mov_b32 m0, s44
	s_nop 0
	global_load_lds_dwordx4 v[146:147], off
	v_lshl_add_u64 v[146:147], v[222:223], 0, s[10:11]
	s_mov_b32 m0, s45
	s_nop 0
	global_load_lds_dwordx4 v[146:147], off
	s_waitcnt vmcnt(8)
	s_waitcnt lgkmcnt(0)
	s_setprio 1
	s_barrier
	v_mfma_f32_16x16x32_bf16 v[62:65], v[154:157], v[186:189], v[62:65]
	v_mfma_f32_16x16x32_bf16 v[58:61], v[162:165], v[186:189], v[58:61]
	v_mfma_f32_16x16x32_bf16 v[54:57], v[154:157], v[194:197], v[54:57]
	v_mfma_f32_16x16x32_bf16 v[46:49], v[162:165], v[194:197], v[46:49]
	v_mfma_f32_16x16x32_bf16 v[38:41], v[154:157], v[202:205], v[38:41]
	v_mfma_f32_16x16x32_bf16 v[30:33], v[162:165], v[202:205], v[30:33]
	v_mfma_f32_16x16x32_bf16 v[22:25], v[154:157], v[210:213], v[22:25]
	v_mfma_f32_16x16x32_bf16 v[14:17], v[162:165], v[210:213], v[14:17]
	v_mfma_f32_16x16x32_bf16 v[62:65], v[158:161], v[190:193], v[62:65]
	v_mfma_f32_16x16x32_bf16 v[58:61], v[166:169], v[190:193], v[58:61]
	v_mfma_f32_16x16x32_bf16 v[54:57], v[158:161], v[198:201], v[54:57]
	v_mfma_f32_16x16x32_bf16 v[46:49], v[166:169], v[198:201], v[46:49]
	v_mfma_f32_16x16x32_bf16 v[38:41], v[158:161], v[206:209], v[38:41]
	v_mfma_f32_16x16x32_bf16 v[30:33], v[166:169], v[206:209], v[30:33]
	v_mfma_f32_16x16x32_bf16 v[22:25], v[158:161], v[214:217], v[22:25]
	v_mfma_f32_16x16x32_bf16 v[14:17], v[166:169], v[214:217], v[14:17]
	s_setprio 0
	s_setprio 1
	v_mfma_f32_16x16x32_bf16 v[50:53], v[170:173], v[186:189], v[50:53]
	v_mfma_f32_16x16x32_bf16 v[42:45], v[178:181], v[186:189], v[42:45]
	v_mfma_f32_16x16x32_bf16 v[34:37], v[170:173], v[194:197], v[34:37]
	v_mfma_f32_16x16x32_bf16 v[26:29], v[178:181], v[194:197], v[26:29]
	v_mfma_f32_16x16x32_bf16 v[18:21], v[170:173], v[202:205], v[18:21]
	v_mfma_f32_16x16x32_bf16 v[10:13], v[178:181], v[202:205], v[10:13]
	v_mfma_f32_16x16x32_bf16 v[6:9], v[170:173], v[210:213], v[6:9]
	v_mfma_f32_16x16x32_bf16 v[2:5], v[178:181], v[210:213], v[2:5]
	v_mfma_f32_16x16x32_bf16 v[50:53], v[174:177], v[190:193], v[50:53]
	v_mfma_f32_16x16x32_bf16 v[42:45], v[182:185], v[190:193], v[42:45]
	v_mfma_f32_16x16x32_bf16 v[34:37], v[174:177], v[198:201], v[34:37]
	v_mfma_f32_16x16x32_bf16 v[26:29], v[182:185], v[198:201], v[26:29]
	v_mfma_f32_16x16x32_bf16 v[18:21], v[174:177], v[206:209], v[18:21]
	v_mfma_f32_16x16x32_bf16 v[10:13], v[182:185], v[206:209], v[10:13]
	v_mfma_f32_16x16x32_bf16 v[6:9], v[174:177], v[214:217], v[6:9]
	v_mfma_f32_16x16x32_bf16 v[2:5], v[182:185], v[214:217], v[2:5]
	s_barrier
	s_setprio 0
	s_add_i32 s59, s59, 2
	s_add_u32 s26, s26, 0x100
	s_addc_u32 s27, s27, 0
	s_add_u32 s57, s57, 0x100
	s_addc_u32 s58, s58, 0
	s_cmpk_gt_u32 s59, 0x55
	s_cbranch_scc0 .LBB0_1562
	s_and_b64 vcc, exec, s[12:13]
	s_cbranch_vccz .LBB0_1565
	s_barrier

.LBB0_1697:
	ds_read_b128 v[156:159], v176
	ds_read_b128 v[160:163], v176 offset:1024
	ds_read_b128 v[164:167], v176 offset:2048
	ds_read_b128 v[168:171], v176 offset:3072
	ds_read_b128 v[180:183], v177
	ds_read_b128 v[184:187], v177 offset:1024
	ds_read_b128 v[188:191], v177 offset:2048
	ds_read_b128 v[192:195], v177 offset:3072
	s_add_u32 s48, s46, 0xfff80080
	s_addc_u32 s49, s47, -1
	s_cmp_eq_u32 s71, 28
	s_cselect_b32 s51, s37, s49
	s_cselect_b32 s50, s43, s48
	s_cselect_b32 s49, s35, s70
	s_cselect_b32 s48, s45, s69
	v_lshl_add_u64 v[172:173], s[46:47], 0, v[148:149]
	s_add_i32 m0, s53, 0xc000
	ds_read_b128 v[196:199], v178
	ds_read_b128 v[200:203], v178 offset:1024
	ds_read_b128 v[204:207], v178 offset:2048
	ds_read_b128 v[208:211], v178 offset:3072
	ds_read_b128 v[212:215], v178 offset:4096
	ds_read_b128 v[216:219], v178 offset:5120
	ds_read_b128 v[220:223], v178 offset:6144
	ds_read_b128 v[224:227], v178 offset:7168
	global_load_lds_dwordx4 v[172:173], off
	v_lshl_add_u64 v[172:173], s[46:47], 0, v[150:151]
	s_add_i32 m0, s53, 0xe000
	s_nop 0
	global_load_lds_dwordx4 v[172:173], off
	s_waitcnt vmcnt(8)
	s_waitcnt lgkmcnt(0)
	s_setprio 1
	s_barrier
	v_mfma_f32_16x16x32_bf16 v[126:129], v[156:159], v[196:199], v[126:129]
	v_mfma_f32_16x16x32_bf16 v[122:125], v[164:167], v[196:199], v[122:125]
	v_mfma_f32_16x16x32_bf16 v[118:121], v[156:159], v[204:207], v[118:121]
	v_mfma_f32_16x16x32_bf16 v[114:117], v[164:167], v[204:207], v[114:117]
	v_mfma_f32_16x16x32_bf16 v[110:113], v[156:159], v[212:215], v[110:113]
	v_mfma_f32_16x16x32_bf16 v[106:109], v[164:167], v[212:215], v[106:109]
	v_mfma_f32_16x16x32_bf16 v[102:105], v[156:159], v[220:223], v[102:105]
	v_mfma_f32_16x16x32_bf16 v[98:101], v[164:167], v[220:223], v[98:101]
	v_mfma_f32_16x16x32_bf16 v[126:129], v[160:163], v[200:203], v[126:129]
	v_mfma_f32_16x16x32_bf16 v[122:125], v[168:171], v[200:203], v[122:125]
	v_mfma_f32_16x16x32_bf16 v[118:121], v[160:163], v[208:211], v[118:121]
	v_mfma_f32_16x16x32_bf16 v[114:117], v[168:171], v[208:211], v[114:117]
	v_mfma_f32_16x16x32_bf16 v[110:113], v[160:163], v[216:219], v[110:113]
	v_mfma_f32_16x16x32_bf16 v[106:109], v[168:171], v[216:219], v[106:109]
	v_mfma_f32_16x16x32_bf16 v[102:105], v[160:163], v[224:227], v[102:105]
	v_mfma_f32_16x16x32_bf16 v[98:101], v[168:171], v[224:227], v[98:101]
	s_setprio 0
	s_setprio 1
	v_mfma_f32_16x16x32_bf16 v[38:41], v[180:183], v[196:199], v[38:41]
	v_mfma_f32_16x16x32_bf16 v[34:37], v[188:191], v[196:199], v[34:37]
	v_mfma_f32_16x16x32_bf16 v[46:49], v[180:183], v[204:207], v[46:49]
	v_mfma_f32_16x16x32_bf16 v[42:45], v[188:191], v[204:207], v[42:45]
	v_mfma_f32_16x16x32_bf16 v[54:57], v[180:183], v[212:215], v[54:57]
	v_mfma_f32_16x16x32_bf16 v[50:53], v[188:191], v[212:215], v[50:53]
	v_mfma_f32_16x16x32_bf16 v[62:65], v[180:183], v[220:223], v[62:65]
	v_mfma_f32_16x16x32_bf16 v[58:61], v[188:191], v[220:223], v[58:61]
	v_mfma_f32_16x16x32_bf16 v[38:41], v[184:187], v[200:203], v[38:41]
	v_mfma_f32_16x16x32_bf16 v[34:37], v[192:195], v[200:203], v[34:37]
	v_mfma_f32_16x16x32_bf16 v[46:49], v[184:187], v[208:211], v[46:49]
	v_mfma_f32_16x16x32_bf16 v[42:45], v[192:195], v[208:211], v[42:45]
	v_mfma_f32_16x16x32_bf16 v[54:57], v[184:187], v[216:219], v[54:57]
	v_mfma_f32_16x16x32_bf16 v[50:53], v[192:195], v[216:219], v[50:53]
	v_mfma_f32_16x16x32_bf16 v[62:65], v[184:187], v[224:227], v[62:65]
	v_mfma_f32_16x16x32_bf16 v[58:61], v[192:195], v[224:227], v[58:61]
	s_barrier
	s_setprio 0
	s_add_i32 s72, s65, s52
	v_lshl_add_u64 v[172:173], s[48:49], 0, v[132:133]
	s_mov_b32 m0, s72
	ds_read_b128 v[196:199], v178 offset:16384
	ds_read_b128 v[200:203], v178 offset:17408
	ds_read_b128 v[204:207], v178 offset:18432
	ds_read_b128 v[208:211], v178 offset:19456
	ds_read_b128 v[212:215], v178 offset:20480
	ds_read_b128 v[216:219], v178 offset:21504
	ds_read_b128 v[220:223], v178 offset:22528
	ds_read_b128 v[224:227], v178 offset:23552
	global_load_lds_dwordx4 v[172:173], off
	s_add_i32 m0, s72, 0x2000
	s_add_u32 s72, s48, 0x80000
	v_lshl_add_u64 v[228:229], s[48:49], 0, v[136:137]
	s_addc_u32 s73, s49, 0
	s_add_i32 s74, s66, s52
	global_load_lds_dwordx4 v[228:229], off
	v_lshl_add_u64 v[230:231], s[72:73], 0, v[132:133]
	s_mov_b32 m0, s74
	v_lshl_add_u64 v[232:233], s[50:51], 0, v[134:135]
	global_load_lds_dwordx4 v[230:231], off
	v_lshl_add_u64 v[230:231], s[72:73], 0, v[136:137]
	s_add_i32 m0, s74, 0x2000
	s_nop 0
	global_load_lds_dwordx4 v[230:231], off
	v_lshl_add_u64 v[230:231], s[50:51], 0, v[130:131]
	s_mov_b32 m0, s53
	s_nop 0
	global_load_lds_dwordx4 v[230:231], off
	s_mov_b32 m0, s54
	s_nop 0
	global_load_lds_dwordx4 v[232:233], off
	s_waitcnt vmcnt(8)
	s_waitcnt lgkmcnt(0)
	s_setprio 1
	s_barrier
	v_mfma_f32_16x16x32_bf16 v[94:97], v[156:159], v[196:199], v[94:97]
	v_mfma_f32_16x16x32_bf16 v[90:93], v[164:167], v[196:199], v[90:93]
	v_mfma_f32_16x16x32_bf16 v[86:89], v[156:159], v[204:207], v[86:89]
	v_mfma_f32_16x16x32_bf16 v[82:85], v[164:167], v[204:207], v[82:85]
	v_mfma_f32_16x16x32_bf16 v[78:81], v[156:159], v[212:215], v[78:81]
	v_mfma_f32_16x16x32_bf16 v[74:77], v[164:167], v[212:215], v[74:77]
	v_mfma_f32_16x16x32_bf16 v[70:73], v[156:159], v[220:223], v[70:73]
	v_mfma_f32_16x16x32_bf16 v[66:69], v[164:167], v[220:223], v[66:69]
	v_mfma_f32_16x16x32_bf16 v[94:97], v[160:163], v[200:203], v[94:97]
	v_mfma_f32_16x16x32_bf16 v[90:93], v[168:171], v[200:203], v[90:93]
	v_mfma_f32_16x16x32_bf16 v[86:89], v[160:163], v[208:211], v[86:89]
	v_mfma_f32_16x16x32_bf16 v[82:85], v[168:171], v[208:211], v[82:85]
	v_mfma_f32_16x16x32_bf16 v[78:81], v[160:163], v[216:219], v[78:81]
	v_mfma_f32_16x16x32_bf16 v[74:77], v[168:171], v[216:219], v[74:77]
	v_mfma_f32_16x16x32_bf16 v[70:73], v[160:163], v[224:227], v[70:73]
	v_mfma_f32_16x16x32_bf16 v[66:69], v[168:171], v[224:227], v[66:69]
	s_setprio 0
	s_setprio 1
	v_mfma_f32_16x16x32_bf16 v[6:9], v[180:183], v[196:199], v[6:9]
	v_mfma_f32_16x16x32_bf16 v[2:5], v[188:191], v[196:199], v[2:5]
	v_mfma_f32_16x16x32_bf16 v[18:21], v[180:183], v[204:207], v[18:21]
	v_mfma_f32_16x16x32_bf16 v[14:17], v[188:191], v[204:207], v[14:17]
	v_mfma_f32_16x16x32_bf16 v[26:29], v[180:183], v[212:215], v[26:29]
	v_mfma_f32_16x16x32_bf16 v[22:25], v[188:191], v[212:215], v[22:25]
	v_mfma_f32_16x16x32_bf16 v[30:33], v[180:183], v[220:223], v[30:33]
	v_mfma_f32_16x16x32_bf16 v[10:13], v[188:191], v[220:223], v[10:13]
	v_mfma_f32_16x16x32_bf16 v[6:9], v[184:187], v[200:203], v[6:9]
	v_mfma_f32_16x16x32_bf16 v[2:5], v[192:195], v[200:203], v[2:5]
	v_mfma_f32_16x16x32_bf16 v[18:21], v[184:187], v[208:211], v[18:21]
	v_mfma_f32_16x16x32_bf16 v[14:17], v[192:195], v[208:211], v[14:17]
	v_mfma_f32_16x16x32_bf16 v[26:29], v[184:187], v[216:219], v[26:29]
	v_mfma_f32_16x16x32_bf16 v[22:25], v[192:195], v[216:219], v[22:25]
	v_mfma_f32_16x16x32_bf16 v[30:33], v[184:187], v[224:227], v[30:33]
	v_mfma_f32_16x16x32_bf16 v[10:13], v[192:195], v[224:227], v[10:13]
	s_barrier
	s_setprio 0
	s_add_i32 s72, 0, 0x18000
	v_add_u32_e32 v138, s72, v174
	s_add_i32 s73, 0, 0x1c000
	ds_read_b128 v[156:159], v138
	ds_read_b128 v[160:163], v138 offset:1024
	ds_read_b128 v[164:167], v138 offset:2048
	ds_read_b128 v[168:171], v138 offset:3072
	v_add_u32_e32 v138, s73, v174
	ds_read_b128 v[180:183], v138
	ds_read_b128 v[184:187], v138 offset:1024
	ds_read_b128 v[188:191], v138 offset:2048
	ds_read_b128 v[192:195], v138 offset:3072
	s_add_u32 s50, s50, 0x80000
	s_addc_u32 s51, s51, 0
	s_mov_b32 m0, s55
	v_lshl_add_u64 v[234:235], s[50:51], 0, v[130:131]
	ds_read_b128 v[196:199], v178 offset:32768
	ds_read_b128 v[200:203], v178 offset:33792
	ds_read_b128 v[204:207], v178 offset:34816
	ds_read_b128 v[208:211], v178 offset:35840
	ds_read_b128 v[212:215], v178 offset:36864
	ds_read_b128 v[216:219], v178 offset:37888
	ds_read_b128 v[220:223], v178 offset:38912
	ds_read_b128 v[224:227], v178 offset:39936
	global_load_lds_dwordx4 v[234:235], off
	v_lshl_add_u64 v[234:235], s[50:51], 0, v[134:135]
	s_mov_b32 m0, s56
	s_nop 0
	global_load_lds_dwordx4 v[234:235], off
	s_waitcnt vmcnt(8)
	s_waitcnt lgkmcnt(0)
	s_setprio 1
	s_barrier
	v_mfma_f32_16x16x32_bf16 v[126:129], v[156:159], v[196:199], v[126:129]
	v_mfma_f32_16x16x32_bf16 v[122:125], v[164:167], v[196:199], v[122:125]
	v_mfma_f32_16x16x32_bf16 v[118:121], v[156:159], v[204:207], v[118:121]
	v_mfma_f32_16x16x32_bf16 v[114:117], v[164:167], v[204:207], v[114:117]
	v_mfma_f32_16x16x32_bf16 v[110:113], v[156:159], v[212:215], v[110:113]
	v_mfma_f32_16x16x32_bf16 v[106:109], v[164:167], v[212:215], v[106:109]
	v_mfma_f32_16x16x32_bf16 v[102:105], v[156:159], v[220:223], v[102:105]
	v_mfma_f32_16x16x32_bf16 v[98:101], v[164:167], v[220:223], v[98:101]
	v_mfma_f32_16x16x32_bf16 v[126:129], v[160:163], v[200:203], v[126:129]
	v_mfma_f32_16x16x32_bf16 v[122:125], v[168:171], v[200:203], v[122:125]
	v_mfma_f32_16x16x32_bf16 v[118:121], v[160:163], v[208:211], v[118:121]
	v_mfma_f32_16x16x32_bf16 v[114:117], v[168:171], v[208:211], v[114:117]
	v_mfma_f32_16x16x32_bf16 v[110:113], v[160:163], v[216:219], v[110:113]
	v_mfma_f32_16x16x32_bf16 v[106:109], v[168:171], v[216:219], v[106:109]
	v_mfma_f32_16x16x32_bf16 v[102:105], v[160:163], v[224:227], v[102:105]
	v_mfma_f32_16x16x32_bf16 v[98:101], v[168:171], v[224:227], v[98:101]
	s_setprio 0
	s_setprio 1
	v_mfma_f32_16x16x32_bf16 v[38:41], v[180:183], v[196:199], v[38:41]
	v_mfma_f32_16x16x32_bf16 v[34:37], v[188:191], v[196:199], v[34:37]
	v_mfma_f32_16x16x32_bf16 v[46:49], v[180:183], v[204:207], v[46:49]
	v_mfma_f32_16x16x32_bf16 v[42:45], v[188:191], v[204:207], v[42:45]
	v_mfma_f32_16x16x32_bf16 v[54:57], v[180:183], v[212:215], v[54:57]
	v_mfma_f32_16x16x32_bf16 v[50:53], v[188:191], v[212:215], v[50:53]
	v_mfma_f32_16x16x32_bf16 v[62:65], v[180:183], v[220:223], v[62:65]
	v_mfma_f32_16x16x32_bf16 v[58:61], v[188:191], v[220:223], v[58:61]
	v_mfma_f32_16x16x32_bf16 v[38:41], v[184:187], v[200:203], v[38:41]
	v_mfma_f32_16x16x32_bf16 v[34:37], v[192:195], v[200:203], v[34:37]
	v_mfma_f32_16x16x32_bf16 v[46:49], v[184:187], v[208:211], v[46:49]
	v_mfma_f32_16x16x32_bf16 v[42:45], v[192:195], v[208:211], v[42:45]
	v_mfma_f32_16x16x32_bf16 v[54:57], v[184:187], v[216:219], v[54:57]
	v_mfma_f32_16x16x32_bf16 v[50:53], v[192:195], v[216:219], v[50:53]
	v_mfma_f32_16x16x32_bf16 v[62:65], v[184:187], v[224:227], v[62:65]
	v_mfma_f32_16x16x32_bf16 v[58:61], v[192:195], v[224:227], v[58:61]
	s_barrier
	s_setprio 0
	s_add_i32 s50, s72, s52
	v_lshl_add_u64 v[172:173], v[172:173], 0, s[6:7]
	s_mov_b32 m0, s50
	ds_read_b128 v[196:199], v178 offset:49152
	ds_read_b128 v[200:203], v178 offset:50176
	ds_read_b128 v[204:207], v178 offset:51200
	ds_read_b128 v[208:211], v178 offset:52224
	ds_read_b128 v[212:215], v178 offset:53248
	ds_read_b128 v[216:219], v178 offset:54272
	ds_read_b128 v[220:223], v178 offset:55296
	ds_read_b128 v[224:227], v178 offset:56320
	global_load_lds_dwordx4 v[172:173], off
	s_add_i32 m0, s50, 0x2000
	s_add_u32 s48, s48, 0x80080
	v_lshl_add_u64 v[172:173], v[228:229], 0, s[6:7]
	s_addc_u32 s49, s49, 0
	s_add_i32 s50, s73, s52
	global_load_lds_dwordx4 v[172:173], off
	v_lshl_add_u64 v[172:173], s[48:49], 0, v[132:133]
	s_mov_b32 m0, s50
	s_nop 0
	global_load_lds_dwordx4 v[172:173], off
	v_lshl_add_u64 v[172:173], s[48:49], 0, v[136:137]
	s_add_i32 m0, s50, 0x2000
	s_nop 0
	global_load_lds_dwordx4 v[172:173], off
	v_lshl_add_u64 v[172:173], v[230:231], 0, s[6:7]
	s_mov_b32 m0, s61
	s_nop 0
	global_load_lds_dwordx4 v[172:173], off
	v_lshl_add_u64 v[172:173], v[232:233], 0, s[6:7]
	s_mov_b32 m0, s62
	s_nop 0
	global_load_lds_dwordx4 v[172:173], off
	s_waitcnt vmcnt(8)
	s_waitcnt lgkmcnt(0)
	s_setprio 1
	s_barrier
	v_mfma_f32_16x16x32_bf16 v[94:97], v[156:159], v[196:199], v[94:97]
	v_mfma_f32_16x16x32_bf16 v[90:93], v[164:167], v[196:199], v[90:93]
	v_mfma_f32_16x16x32_bf16 v[86:89], v[156:159], v[204:207], v[86:89]
	v_mfma_f32_16x16x32_bf16 v[82:85], v[164:167], v[204:207], v[82:85]
	v_mfma_f32_16x16x32_bf16 v[78:81], v[156:159], v[212:215], v[78:81]
	v_mfma_f32_16x16x32_bf16 v[74:77], v[164:167], v[212:215], v[74:77]
	v_mfma_f32_16x16x32_bf16 v[70:73], v[156:159], v[220:223], v[70:73]
	v_mfma_f32_16x16x32_bf16 v[66:69], v[164:167], v[220:223], v[66:69]
	v_mfma_f32_16x16x32_bf16 v[94:97], v[160:163], v[200:203], v[94:97]
	v_mfma_f32_16x16x32_bf16 v[90:93], v[168:171], v[200:203], v[90:93]
	v_mfma_f32_16x16x32_bf16 v[86:89], v[160:163], v[208:211], v[86:89]
	v_mfma_f32_16x16x32_bf16 v[82:85], v[168:171], v[208:211], v[82:85]
	v_mfma_f32_16x16x32_bf16 v[78:81], v[160:163], v[216:219], v[78:81]
	v_mfma_f32_16x16x32_bf16 v[74:77], v[168:171], v[216:219], v[74:77]
	v_mfma_f32_16x16x32_bf16 v[70:73], v[160:163], v[224:227], v[70:73]
	v_mfma_f32_16x16x32_bf16 v[66:69], v[168:171], v[224:227], v[66:69]
	s_setprio 0
	s_setprio 1
	v_mfma_f32_16x16x32_bf16 v[6:9], v[180:183], v[196:199], v[6:9]
	v_mfma_f32_16x16x32_bf16 v[2:5], v[188:191], v[196:199], v[2:5]
	v_mfma_f32_16x16x32_bf16 v[18:21], v[180:183], v[204:207], v[18:21]
	v_mfma_f32_16x16x32_bf16 v[14:17], v[188:191], v[204:207], v[14:17]
	v_mfma_f32_16x16x32_bf16 v[26:29], v[180:183], v[212:215], v[26:29]
	v_mfma_f32_16x16x32_bf16 v[22:25], v[188:191], v[212:215], v[22:25]
	v_mfma_f32_16x16x32_bf16 v[30:33], v[180:183], v[220:223], v[30:33]
	v_mfma_f32_16x16x32_bf16 v[10:13], v[188:191], v[220:223], v[10:13]
	v_mfma_f32_16x16x32_bf16 v[6:9], v[184:187], v[200:203], v[6:9]
	v_mfma_f32_16x16x32_bf16 v[2:5], v[192:195], v[200:203], v[2:5]
	v_mfma_f32_16x16x32_bf16 v[18:21], v[184:187], v[208:211], v[18:21]
	v_mfma_f32_16x16x32_bf16 v[14:17], v[192:195], v[208:211], v[14:17]
	v_mfma_f32_16x16x32_bf16 v[26:29], v[184:187], v[216:219], v[26:29]
	v_mfma_f32_16x16x32_bf16 v[22:25], v[192:195], v[216:219], v[22:25]
	v_mfma_f32_16x16x32_bf16 v[30:33], v[184:187], v[224:227], v[30:33]
	v_mfma_f32_16x16x32_bf16 v[10:13], v[192:195], v[224:227], v[10:13]
	s_barrier
	s_setprio 0
	s_add_i32 s71, s71, 2
	s_add_u32 s46, s46, 0x100
	s_addc_u32 s47, s47, 0
	s_add_u32 s69, s69, 0x100
	s_addc_u32 s70, s70, 0
	s_cmp_gt_u32 s71, 29
	s_cbranch_scc0 .LBB0_1697
	s_and_b64 vcc, exec, s[12:13]
	s_cbranch_vccz .LBB0_1700
	s_barrier

.LBB0_2114:
	ds_read_b128 v[154:157], v150
	ds_read_b128 v[158:161], v150 offset:1024
	ds_read_b128 v[162:165], v150 offset:2048
	ds_read_b128 v[166:169], v150 offset:3072
	ds_read_b128 v[170:173], v151
	ds_read_b128 v[174:177], v151 offset:1024
	ds_read_b128 v[178:181], v151 offset:2048
	ds_read_b128 v[182:185], v151 offset:3072
	s_add_u32 s36, s34, 0xfff80080
	s_addc_u32 s37, s35, -1
	s_cmp_eq_u32 s61, 28
	s_cselect_b32 s39, s25, s37
	s_cselect_b32 s38, s57, s36
	s_cselect_b32 s37, s23, s60
	s_cselect_b32 s36, s58, s59
	v_lshl_add_u64 v[146:147], s[34:35], 0, v[138:139]
	s_add_i32 m0, s31, 0xc000
	ds_read_b128 v[186:189], v152
	ds_read_b128 v[190:193], v152 offset:1024
	ds_read_b128 v[194:197], v152 offset:2048
	ds_read_b128 v[198:201], v152 offset:3072
	ds_read_b128 v[202:205], v152 offset:4096
	ds_read_b128 v[206:209], v152 offset:5120
	ds_read_b128 v[210:213], v152 offset:6144
	ds_read_b128 v[214:217], v152 offset:7168
	global_load_lds_dwordx4 v[146:147], off
	v_lshl_add_u64 v[146:147], s[34:35], 0, v[140:141]
	s_add_i32 m0, s31, 0xe000
	s_nop 0
	global_load_lds_dwordx4 v[146:147], off
	s_waitcnt vmcnt(8)
	s_waitcnt lgkmcnt(0)
	s_setprio 1
	s_barrier
	v_mfma_f32_16x16x32_bf16 v[126:129], v[154:157], v[186:189], v[126:129]
	v_mfma_f32_16x16x32_bf16 v[122:125], v[162:165], v[186:189], v[122:125]
	v_mfma_f32_16x16x32_bf16 v[118:121], v[154:157], v[194:197], v[118:121]
	v_mfma_f32_16x16x32_bf16 v[110:113], v[162:165], v[194:197], v[110:113]
	v_mfma_f32_16x16x32_bf16 v[102:105], v[154:157], v[202:205], v[102:105]
	v_mfma_f32_16x16x32_bf16 v[94:97], v[162:165], v[202:205], v[94:97]
	v_mfma_f32_16x16x32_bf16 v[86:89], v[154:157], v[210:213], v[86:89]
	v_mfma_f32_16x16x32_bf16 v[78:81], v[162:165], v[210:213], v[78:81]
	v_mfma_f32_16x16x32_bf16 v[126:129], v[158:161], v[190:193], v[126:129]
	v_mfma_f32_16x16x32_bf16 v[122:125], v[166:169], v[190:193], v[122:125]
	v_mfma_f32_16x16x32_bf16 v[118:121], v[158:161], v[198:201], v[118:121]
	v_mfma_f32_16x16x32_bf16 v[110:113], v[166:169], v[198:201], v[110:113]
	v_mfma_f32_16x16x32_bf16 v[102:105], v[158:161], v[206:209], v[102:105]
	v_mfma_f32_16x16x32_bf16 v[94:97], v[166:169], v[206:209], v[94:97]
	v_mfma_f32_16x16x32_bf16 v[86:89], v[158:161], v[214:217], v[86:89]
	v_mfma_f32_16x16x32_bf16 v[78:81], v[166:169], v[214:217], v[78:81]
	s_setprio 0
	s_setprio 1
	v_mfma_f32_16x16x32_bf16 v[114:117], v[170:173], v[186:189], v[114:117]
	v_mfma_f32_16x16x32_bf16 v[106:109], v[178:181], v[186:189], v[106:109]
	v_mfma_f32_16x16x32_bf16 v[98:101], v[170:173], v[194:197], v[98:101]
	v_mfma_f32_16x16x32_bf16 v[90:93], v[178:181], v[194:197], v[90:93]
	v_mfma_f32_16x16x32_bf16 v[82:85], v[170:173], v[202:205], v[82:85]
	v_mfma_f32_16x16x32_bf16 v[74:77], v[178:181], v[202:205], v[74:77]
	v_mfma_f32_16x16x32_bf16 v[70:73], v[170:173], v[210:213], v[70:73]
	v_mfma_f32_16x16x32_bf16 v[66:69], v[178:181], v[210:213], v[66:69]
	v_mfma_f32_16x16x32_bf16 v[114:117], v[174:177], v[190:193], v[114:117]
	v_mfma_f32_16x16x32_bf16 v[106:109], v[182:185], v[190:193], v[106:109]
	v_mfma_f32_16x16x32_bf16 v[98:101], v[174:177], v[198:201], v[98:101]
	v_mfma_f32_16x16x32_bf16 v[90:93], v[182:185], v[198:201], v[90:93]
	v_mfma_f32_16x16x32_bf16 v[82:85], v[174:177], v[206:209], v[82:85]
	v_mfma_f32_16x16x32_bf16 v[74:77], v[182:185], v[206:209], v[74:77]
	v_mfma_f32_16x16x32_bf16 v[70:73], v[174:177], v[214:217], v[70:73]
	v_mfma_f32_16x16x32_bf16 v[66:69], v[182:185], v[214:217], v[66:69]
	s_barrier
	s_setprio 0
	s_add_i32 s62, s50, s42
	v_lshl_add_u64 v[146:147], s[36:37], 0, v[132:133]
	s_mov_b32 m0, s62
	ds_read_b128 v[186:189], v152 offset:16384
	ds_read_b128 v[190:193], v152 offset:17408
	ds_read_b128 v[194:197], v152 offset:18432
	ds_read_b128 v[198:201], v152 offset:19456
	ds_read_b128 v[202:205], v152 offset:20480
	ds_read_b128 v[206:209], v152 offset:21504
	ds_read_b128 v[210:213], v152 offset:22528
	ds_read_b128 v[214:217], v152 offset:23552
	global_load_lds_dwordx4 v[146:147], off
	s_add_i32 m0, s62, 0x2000
	s_add_u32 s62, s36, 0x80000
	v_lshl_add_u64 v[218:219], s[36:37], 0, v[136:137]
	s_addc_u32 s63, s37, 0
	s_add_i32 s64, s51, s42
	global_load_lds_dwordx4 v[218:219], off
	v_lshl_add_u64 v[220:221], s[62:63], 0, v[132:133]
	s_mov_b32 m0, s64
	v_lshl_add_u64 v[222:223], s[38:39], 0, v[134:135]
	global_load_lds_dwordx4 v[220:221], off
	v_lshl_add_u64 v[220:221], s[62:63], 0, v[136:137]
	s_add_i32 m0, s64, 0x2000
	s_nop 0
	global_load_lds_dwordx4 v[220:221], off
	v_lshl_add_u64 v[220:221], s[38:39], 0, v[130:131]
	s_mov_b32 m0, s31
	s_nop 0
	global_load_lds_dwordx4 v[220:221], off
	s_mov_b32 m0, s43
	s_nop 0
	global_load_lds_dwordx4 v[222:223], off
	s_waitcnt vmcnt(8)
	s_waitcnt lgkmcnt(0)
	s_setprio 1
	s_barrier
	v_mfma_f32_16x16x32_bf16 v[62:65], v[154:157], v[186:189], v[62:65]
	v_mfma_f32_16x16x32_bf16 v[58:61], v[162:165], v[186:189], v[58:61]
	v_mfma_f32_16x16x32_bf16 v[54:57], v[154:157], v[194:197], v[54:57]
	v_mfma_f32_16x16x32_bf16 v[46:49], v[162:165], v[194:197], v[46:49]
	v_mfma_f32_16x16x32_bf16 v[38:41], v[154:157], v[202:205], v[38:41]
	v_mfma_f32_16x16x32_bf16 v[30:33], v[162:165], v[202:205], v[30:33]
	v_mfma_f32_16x16x32_bf16 v[22:25], v[154:157], v[210:213], v[22:25]
	v_mfma_f32_16x16x32_bf16 v[14:17], v[162:165], v[210:213], v[14:17]
	v_mfma_f32_16x16x32_bf16 v[62:65], v[158:161], v[190:193], v[62:65]
	v_mfma_f32_16x16x32_bf16 v[58:61], v[166:169], v[190:193], v[58:61]
	v_mfma_f32_16x16x32_bf16 v[54:57], v[158:161], v[198:201], v[54:57]
	v_mfma_f32_16x16x32_bf16 v[46:49], v[166:169], v[198:201], v[46:49]
	v_mfma_f32_16x16x32_bf16 v[38:41], v[158:161], v[206:209], v[38:41]
	v_mfma_f32_16x16x32_bf16 v[30:33], v[166:169], v[206:209], v[30:33]
	v_mfma_f32_16x16x32_bf16 v[22:25], v[158:161], v[214:217], v[22:25]
	v_mfma_f32_16x16x32_bf16 v[14:17], v[166:169], v[214:217], v[14:17]
	s_setprio 0
	s_setprio 1
	v_mfma_f32_16x16x32_bf16 v[50:53], v[170:173], v[186:189], v[50:53]
	v_mfma_f32_16x16x32_bf16 v[42:45], v[178:181], v[186:189], v[42:45]
	v_mfma_f32_16x16x32_bf16 v[34:37], v[170:173], v[194:197], v[34:37]
	v_mfma_f32_16x16x32_bf16 v[26:29], v[178:181], v[194:197], v[26:29]
	v_mfma_f32_16x16x32_bf16 v[18:21], v[170:173], v[202:205], v[18:21]
	v_mfma_f32_16x16x32_bf16 v[10:13], v[178:181], v[202:205], v[10:13]
	v_mfma_f32_16x16x32_bf16 v[6:9], v[170:173], v[210:213], v[6:9]
	v_mfma_f32_16x16x32_bf16 v[2:5], v[178:181], v[210:213], v[2:5]
	v_mfma_f32_16x16x32_bf16 v[50:53], v[174:177], v[190:193], v[50:53]
	v_mfma_f32_16x16x32_bf16 v[42:45], v[182:185], v[190:193], v[42:45]
	v_mfma_f32_16x16x32_bf16 v[34:37], v[174:177], v[198:201], v[34:37]
	v_mfma_f32_16x16x32_bf16 v[26:29], v[182:185], v[198:201], v[26:29]
	v_mfma_f32_16x16x32_bf16 v[18:21], v[174:177], v[206:209], v[18:21]
	v_mfma_f32_16x16x32_bf16 v[10:13], v[182:185], v[206:209], v[10:13]
	v_mfma_f32_16x16x32_bf16 v[6:9], v[174:177], v[214:217], v[6:9]
	v_mfma_f32_16x16x32_bf16 v[2:5], v[182:185], v[214:217], v[2:5]
	s_barrier
	s_setprio 0
	s_add_i32 s62, 0, 0x18000
	v_add_u32_e32 v153, s62, v148
	s_add_i32 s63, 0, 0x1c000
	ds_read_b128 v[154:157], v153
	ds_read_b128 v[158:161], v153 offset:1024
	ds_read_b128 v[162:165], v153 offset:2048
	ds_read_b128 v[166:169], v153 offset:3072
	v_add_u32_e32 v153, s63, v148
	ds_read_b128 v[170:173], v153
	ds_read_b128 v[174:177], v153 offset:1024
	ds_read_b128 v[178:181], v153 offset:2048
	ds_read_b128 v[182:185], v153 offset:3072
	s_add_u32 s38, s38, 0x80000
	s_addc_u32 s39, s39, 0
	s_mov_b32 m0, s44
	v_lshl_add_u64 v[224:225], s[38:39], 0, v[130:131]
	ds_read_b128 v[186:189], v152 offset:32768
	ds_read_b128 v[190:193], v152 offset:33792
	ds_read_b128 v[194:197], v152 offset:34816
	ds_read_b128 v[198:201], v152 offset:35840
	ds_read_b128 v[202:205], v152 offset:36864
	ds_read_b128 v[206:209], v152 offset:37888
	ds_read_b128 v[210:213], v152 offset:38912
	ds_read_b128 v[214:217], v152 offset:39936
	global_load_lds_dwordx4 v[224:225], off
	v_lshl_add_u64 v[224:225], s[38:39], 0, v[134:135]
	s_mov_b32 m0, s45
	s_nop 0
	global_load_lds_dwordx4 v[224:225], off
	s_waitcnt vmcnt(8)
	s_waitcnt lgkmcnt(0)
	s_setprio 1
	s_barrier
	v_mfma_f32_16x16x32_bf16 v[126:129], v[154:157], v[186:189], v[126:129]
	v_mfma_f32_16x16x32_bf16 v[122:125], v[162:165], v[186:189], v[122:125]
	v_mfma_f32_16x16x32_bf16 v[118:121], v[154:157], v[194:197], v[118:121]
	v_mfma_f32_16x16x32_bf16 v[110:113], v[162:165], v[194:197], v[110:113]
	v_mfma_f32_16x16x32_bf16 v[102:105], v[154:157], v[202:205], v[102:105]
	v_mfma_f32_16x16x32_bf16 v[94:97], v[162:165], v[202:205], v[94:97]
	v_mfma_f32_16x16x32_bf16 v[86:89], v[154:157], v[210:213], v[86:89]
	v_mfma_f32_16x16x32_bf16 v[78:81], v[162:165], v[210:213], v[78:81]
	v_mfma_f32_16x16x32_bf16 v[126:129], v[158:161], v[190:193], v[126:129]
	v_mfma_f32_16x16x32_bf16 v[122:125], v[166:169], v[190:193], v[122:125]
	v_mfma_f32_16x16x32_bf16 v[118:121], v[158:161], v[198:201], v[118:121]
	v_mfma_f32_16x16x32_bf16 v[110:113], v[166:169], v[198:201], v[110:113]
	v_mfma_f32_16x16x32_bf16 v[102:105], v[158:161], v[206:209], v[102:105]
	v_mfma_f32_16x16x32_bf16 v[94:97], v[166:169], v[206:209], v[94:97]
	v_mfma_f32_16x16x32_bf16 v[86:89], v[158:161], v[214:217], v[86:89]
	v_mfma_f32_16x16x32_bf16 v[78:81], v[166:169], v[214:217], v[78:81]
	s_setprio 0
	s_setprio 1
	v_mfma_f32_16x16x32_bf16 v[114:117], v[170:173], v[186:189], v[114:117]
	v_mfma_f32_16x16x32_bf16 v[106:109], v[178:181], v[186:189], v[106:109]
	v_mfma_f32_16x16x32_bf16 v[98:101], v[170:173], v[194:197], v[98:101]
	v_mfma_f32_16x16x32_bf16 v[90:93], v[178:181], v[194:197], v[90:93]
	v_mfma_f32_16x16x32_bf16 v[82:85], v[170:173], v[202:205], v[82:85]
	v_mfma_f32_16x16x32_bf16 v[74:77], v[178:181], v[202:205], v[74:77]
	v_mfma_f32_16x16x32_bf16 v[70:73], v[170:173], v[210:213], v[70:73]
	v_mfma_f32_16x16x32_bf16 v[66:69], v[178:181], v[210:213], v[66:69]
	v_mfma_f32_16x16x32_bf16 v[114:117], v[174:177], v[190:193], v[114:117]
	v_mfma_f32_16x16x32_bf16 v[106:109], v[182:185], v[190:193], v[106:109]
	v_mfma_f32_16x16x32_bf16 v[98:101], v[174:177], v[198:201], v[98:101]
	v_mfma_f32_16x16x32_bf16 v[90:93], v[182:185], v[198:201], v[90:93]
	v_mfma_f32_16x16x32_bf16 v[82:85], v[174:177], v[206:209], v[82:85]
	v_mfma_f32_16x16x32_bf16 v[74:77], v[182:185], v[206:209], v[74:77]
	v_mfma_f32_16x16x32_bf16 v[70:73], v[174:177], v[214:217], v[70:73]
	v_mfma_f32_16x16x32_bf16 v[66:69], v[182:185], v[214:217], v[66:69]
	s_barrier
	s_setprio 0
	s_add_i32 s38, s62, s42
	v_lshl_add_u64 v[146:147], v[146:147], 0, s[10:11]
	s_mov_b32 m0, s38
	ds_read_b128 v[186:189], v152 offset:49152
	ds_read_b128 v[190:193], v152 offset:50176
	ds_read_b128 v[194:197], v152 offset:51200
	ds_read_b128 v[198:201], v152 offset:52224
	ds_read_b128 v[202:205], v152 offset:53248
	ds_read_b128 v[206:209], v152 offset:54272
	ds_read_b128 v[210:213], v152 offset:55296
	ds_read_b128 v[214:217], v152 offset:56320
	global_load_lds_dwordx4 v[146:147], off
	s_add_i32 m0, s38, 0x2000
	s_add_u32 s36, s36, 0x80080
	v_lshl_add_u64 v[146:147], v[218:219], 0, s[10:11]
	s_addc_u32 s37, s37, 0
	s_add_i32 s38, s63, s42
	global_load_lds_dwordx4 v[146:147], off
	v_lshl_add_u64 v[146:147], s[36:37], 0, v[132:133]
	s_mov_b32 m0, s38
	s_nop 0
	global_load_lds_dwordx4 v[146:147], off
	v_lshl_add_u64 v[146:147], s[36:37], 0, v[136:137]
	s_add_i32 m0, s38, 0x2000
	s_nop 0
	global_load_lds_dwordx4 v[146:147], off
	v_lshl_add_u64 v[146:147], v[220:221], 0, s[10:11]
	s_mov_b32 m0, s47
	s_nop 0
	global_load_lds_dwordx4 v[146:147], off
	v_lshl_add_u64 v[146:147], v[222:223], 0, s[10:11]
	s_mov_b32 m0, s48
	s_nop 0
	global_load_lds_dwordx4 v[146:147], off
	s_waitcnt vmcnt(8)
	s_waitcnt lgkmcnt(0)
	s_setprio 1
	s_barrier
	v_mfma_f32_16x16x32_bf16 v[62:65], v[154:157], v[186:189], v[62:65]
	v_mfma_f32_16x16x32_bf16 v[58:61], v[162:165], v[186:189], v[58:61]
	v_mfma_f32_16x16x32_bf16 v[54:57], v[154:157], v[194:197], v[54:57]
	v_mfma_f32_16x16x32_bf16 v[46:49], v[162:165], v[194:197], v[46:49]
	v_mfma_f32_16x16x32_bf16 v[38:41], v[154:157], v[202:205], v[38:41]
	v_mfma_f32_16x16x32_bf16 v[30:33], v[162:165], v[202:205], v[30:33]
	v_mfma_f32_16x16x32_bf16 v[22:25], v[154:157], v[210:213], v[22:25]
	v_mfma_f32_16x16x32_bf16 v[14:17], v[162:165], v[210:213], v[14:17]
	v_mfma_f32_16x16x32_bf16 v[62:65], v[158:161], v[190:193], v[62:65]
	v_mfma_f32_16x16x32_bf16 v[58:61], v[166:169], v[190:193], v[58:61]
	v_mfma_f32_16x16x32_bf16 v[54:57], v[158:161], v[198:201], v[54:57]
	v_mfma_f32_16x16x32_bf16 v[46:49], v[166:169], v[198:201], v[46:49]
	v_mfma_f32_16x16x32_bf16 v[38:41], v[158:161], v[206:209], v[38:41]
	v_mfma_f32_16x16x32_bf16 v[30:33], v[166:169], v[206:209], v[30:33]
	v_mfma_f32_16x16x32_bf16 v[22:25], v[158:161], v[214:217], v[22:25]
	v_mfma_f32_16x16x32_bf16 v[14:17], v[166:169], v[214:217], v[14:17]
	s_setprio 0
	s_setprio 1
	v_mfma_f32_16x16x32_bf16 v[50:53], v[170:173], v[186:189], v[50:53]
	v_mfma_f32_16x16x32_bf16 v[42:45], v[178:181], v[186:189], v[42:45]
	v_mfma_f32_16x16x32_bf16 v[34:37], v[170:173], v[194:197], v[34:37]
	v_mfma_f32_16x16x32_bf16 v[26:29], v[178:181], v[194:197], v[26:29]
	v_mfma_f32_16x16x32_bf16 v[18:21], v[170:173], v[202:205], v[18:21]
	v_mfma_f32_16x16x32_bf16 v[10:13], v[178:181], v[202:205], v[10:13]
	v_mfma_f32_16x16x32_bf16 v[6:9], v[170:173], v[210:213], v[6:9]
	v_mfma_f32_16x16x32_bf16 v[2:5], v[178:181], v[210:213], v[2:5]
	v_mfma_f32_16x16x32_bf16 v[50:53], v[174:177], v[190:193], v[50:53]
	v_mfma_f32_16x16x32_bf16 v[42:45], v[182:185], v[190:193], v[42:45]
	v_mfma_f32_16x16x32_bf16 v[34:37], v[174:177], v[198:201], v[34:37]
	v_mfma_f32_16x16x32_bf16 v[26:29], v[182:185], v[198:201], v[26:29]
	v_mfma_f32_16x16x32_bf16 v[18:21], v[174:177], v[206:209], v[18:21]
	v_mfma_f32_16x16x32_bf16 v[10:13], v[182:185], v[206:209], v[10:13]
	v_mfma_f32_16x16x32_bf16 v[6:9], v[174:177], v[214:217], v[6:9]
	v_mfma_f32_16x16x32_bf16 v[2:5], v[182:185], v[214:217], v[2:5]
	s_barrier
	s_setprio 0
	s_add_i32 s61, s61, 2
	s_add_u32 s34, s34, 0x100
	s_addc_u32 s35, s35, 0
	s_add_u32 s59, s59, 0x100
	s_addc_u32 s60, s60, 0
	s_cmp_gt_u32 s61, 29
	s_cbranch_scc0 .LBB0_2114
	s_and_b64 vcc, exec, s[12:13]
	s_cbranch_vccz .LBB0_2117
	s_barrier

.LBB0_2366:
	ds_read_b128 v[18:21], v186
	ds_read_b128 v[22:25], v186 offset:1024
	ds_read_b128 v[26:29], v186 offset:2048
	ds_read_b128 v[30:33], v186 offset:3072
	ds_read_b128 v[2:5], v187
	ds_read_b128 v[6:9], v187 offset:1024
	ds_read_b128 v[10:13], v187 offset:2048
	ds_read_b128 v[14:17], v187 offset:3072
	s_add_u32 s36, s34, 0xfffc0080
	s_addc_u32 s37, s35, -1
	s_cmp_eq_u32 s70, 12
	s_cselect_b32 s39, s23, s37
	s_cselect_b32 s38, s66, s36
	s_cselect_b32 s37, s25, s69
	s_cselect_b32 s36, s67, s68
	v_lshl_add_u64 v[208:209], s[34:35], 0, v[170:171]
	s_add_i32 m0, s31, 0xc000
	ds_read_b128 v[176:179], v188
	ds_read_b128 v[180:183], v188 offset:1024
	ds_read_b128 v[192:195], v188 offset:2048
	ds_read_b128 v[196:199], v188 offset:3072
	ds_read_b128 v[200:203], v188 offset:4096
	ds_read_b128 v[204:207], v188 offset:5120
	ds_read_b128 v[216:219], v188 offset:6144
	ds_read_b128 v[220:223], v188 offset:7168
	global_load_lds_dwordx4 v[208:209], off
	v_lshl_add_u64 v[208:209], s[34:35], 0, v[172:173]
	s_add_i32 m0, s31, 0xe000
	s_nop 0
	global_load_lds_dwordx4 v[208:209], off
	s_waitcnt vmcnt(8)
	s_waitcnt lgkmcnt(0)
	s_setprio 1
	s_barrier
	v_mfma_scale_f32_16x16x128_f8f6f4 v[158:161], v[18:25], v[176:183], v[158:161], v189, v190 op_sel_hi:[0,0,0]
	v_mfma_scale_f32_16x16x128_f8f6f4 v[150:153], v[26:33], v[176:183], v[150:153], v189, v190 op_sel_hi:[0,0,0]
	v_mfma_scale_f32_16x16x128_f8f6f4 v[142:145], v[18:25], v[192:199], v[142:145], v189, v190 op_sel_hi:[0,0,0]
	v_mfma_scale_f32_16x16x128_f8f6f4 v[134:137], v[26:33], v[192:199], v[134:137], v189, v190 op_sel_hi:[0,0,0]
	v_mfma_scale_f32_16x16x128_f8f6f4 v[126:129], v[18:25], v[200:207], v[126:129], v189, v190 op_sel_hi:[0,0,0]
	v_mfma_scale_f32_16x16x128_f8f6f4 v[118:121], v[26:33], v[200:207], v[118:121], v189, v190 op_sel_hi:[0,0,0]
	v_mfma_scale_f32_16x16x128_f8f6f4 v[110:113], v[18:25], v[216:223], v[110:113], v189, v190 op_sel_hi:[0,0,0]
	v_mfma_scale_f32_16x16x128_f8f6f4 v[102:105], v[26:33], v[216:223], v[102:105], v189, v190 op_sel_hi:[0,0,0]
	s_setprio 0
	s_setprio 1
	v_mfma_scale_f32_16x16x128_f8f6f4 v[154:157], v[2:9], v[176:183], v[154:157], v189, v190 op_sel_hi:[0,0,0]
	v_mfma_scale_f32_16x16x128_f8f6f4 v[146:149], v[10:17], v[176:183], v[146:149], v189, v190 op_sel_hi:[0,0,0]
	v_mfma_scale_f32_16x16x128_f8f6f4 v[138:141], v[2:9], v[192:199], v[138:141], v189, v190 op_sel_hi:[0,0,0]
	v_mfma_scale_f32_16x16x128_f8f6f4 v[130:133], v[10:17], v[192:199], v[130:133], v189, v190 op_sel_hi:[0,0,0]
	v_mfma_scale_f32_16x16x128_f8f6f4 v[122:125], v[2:9], v[200:207], v[122:125], v189, v190 op_sel_hi:[0,0,0]
	v_mfma_scale_f32_16x16x128_f8f6f4 v[114:117], v[10:17], v[200:207], v[114:117], v189, v190 op_sel_hi:[0,0,0]
	v_mfma_scale_f32_16x16x128_f8f6f4 v[106:109], v[2:9], v[216:223], v[106:109], v189, v190 op_sel_hi:[0,0,0]
	v_mfma_scale_f32_16x16x128_f8f6f4 v[98:101], v[10:17], v[216:223], v[98:101], v189, v190 op_sel_hi:[0,0,0]
	s_barrier
	s_setprio 0
	s_add_i32 s71, s60, s43
	v_lshl_add_u64 v[176:177], s[36:37], 0, v[166:167]
	s_mov_b32 m0, s71
	ds_read_b128 v[192:195], v188 offset:16384
	ds_read_b128 v[196:199], v188 offset:17408
	ds_read_b128 v[200:203], v188 offset:18432
	ds_read_b128 v[204:207], v188 offset:19456
	ds_read_b128 v[216:219], v188 offset:20480
	ds_read_b128 v[220:223], v188 offset:21504
	ds_read_b128 v[224:227], v188 offset:22528
	ds_read_b128 v[228:231], v188 offset:23552
	global_load_lds_dwordx4 v[176:177], off
	s_add_i32 m0, s71, 0x2000
	s_add_u32 s72, s36, 0x40000
	v_lshl_add_u64 v[178:179], s[36:37], 0, v[162:163]
	s_addc_u32 s73, s37, 0
	s_add_i32 s71, s61, s43
	global_load_lds_dwordx4 v[178:179], off
	v_lshl_add_u64 v[180:181], s[72:73], 0, v[166:167]
	s_mov_b32 m0, s71
	v_lshl_add_u64 v[182:183], s[38:39], 0, v[164:165]
	global_load_lds_dwordx4 v[180:181], off
	v_lshl_add_u64 v[180:181], s[72:73], 0, v[162:163]
	s_add_i32 m0, s71, 0x2000
	s_nop 0
	global_load_lds_dwordx4 v[180:181], off
	v_lshl_add_u64 v[180:181], s[38:39], 0, v[168:169]
	s_mov_b32 m0, s31
	s_nop 0
	global_load_lds_dwordx4 v[180:181], off
	s_mov_b32 m0, s47
	s_nop 0
	global_load_lds_dwordx4 v[182:183], off
	s_waitcnt vmcnt(8)
	s_waitcnt lgkmcnt(0)
	s_setprio 1
	s_barrier
	v_mfma_scale_f32_16x16x128_f8f6f4 v[94:97], v[18:25], v[192:199], v[94:97], v189, v190 op_sel_hi:[0,0,0]
	v_mfma_scale_f32_16x16x128_f8f6f4 v[86:89], v[26:33], v[192:199], v[86:89], v189, v190 op_sel_hi:[0,0,0]
	v_mfma_scale_f32_16x16x128_f8f6f4 v[78:81], v[18:25], v[200:207], v[78:81], v189, v190 op_sel_hi:[0,0,0]
	v_mfma_scale_f32_16x16x128_f8f6f4 v[70:73], v[26:33], v[200:207], v[70:73], v189, v190 op_sel_hi:[0,0,0]
	v_mfma_scale_f32_16x16x128_f8f6f4 v[62:65], v[18:25], v[216:223], v[62:65], v189, v190 op_sel_hi:[0,0,0]
	v_mfma_scale_f32_16x16x128_f8f6f4 v[54:57], v[26:33], v[216:223], v[54:57], v189, v190 op_sel_hi:[0,0,0]
	v_mfma_scale_f32_16x16x128_f8f6f4 v[46:49], v[18:25], v[224:231], v[46:49], v189, v190 op_sel_hi:[0,0,0]
	v_mfma_scale_f32_16x16x128_f8f6f4 v[38:41], v[26:33], v[224:231], v[38:41], v189, v190 op_sel_hi:[0,0,0]
	s_setprio 0
	s_setprio 1
	v_mfma_scale_f32_16x16x128_f8f6f4 v[90:93], v[2:9], v[192:199], v[90:93], v189, v190 op_sel_hi:[0,0,0]
	v_mfma_scale_f32_16x16x128_f8f6f4 v[82:85], v[10:17], v[192:199], v[82:85], v189, v190 op_sel_hi:[0,0,0]
	v_mfma_scale_f32_16x16x128_f8f6f4 v[74:77], v[2:9], v[200:207], v[74:77], v189, v190 op_sel_hi:[0,0,0]
	v_mfma_scale_f32_16x16x128_f8f6f4 v[66:69], v[10:17], v[200:207], v[66:69], v189, v190 op_sel_hi:[0,0,0]
	v_mfma_scale_f32_16x16x128_f8f6f4 v[58:61], v[2:9], v[216:223], v[58:61], v189, v190 op_sel_hi:[0,0,0]
	v_mfma_scale_f32_16x16x128_f8f6f4 v[50:53], v[10:17], v[216:223], v[50:53], v189, v190 op_sel_hi:[0,0,0]
	v_mfma_scale_f32_16x16x128_f8f6f4 v[42:45], v[2:9], v[224:231], v[42:45], v189, v190 op_sel_hi:[0,0,0]
	v_mfma_scale_f32_16x16x128_f8f6f4 v[34:37], v[10:17], v[224:231], v[34:37], v189, v190 op_sel_hi:[0,0,0]
	s_barrier
	s_setprio 0
	s_add_i32 s71, 0, 0x18000
	s_add_i32 s72, 0, 0x1c000
	v_add_u32_e32 v14, s71, v184
	v_add_u32_e32 v30, s72, v184
	ds_read_b128 v[2:5], v14
	ds_read_b128 v[6:9], v14 offset:1024
	ds_read_b128 v[10:13], v14 offset:2048
	ds_read_b128 v[14:17], v14 offset:3072
	ds_read_b128 v[18:21], v30
	ds_read_b128 v[22:25], v30 offset:1024
	ds_read_b128 v[26:29], v30 offset:2048
	ds_read_b128 v[30:33], v30 offset:3072
	s_add_u32 s38, s38, 0x40000
	s_addc_u32 s39, s39, 0
	s_mov_b32 m0, s48
	v_lshl_add_u64 v[208:209], s[38:39], 0, v[168:169]
	ds_read_b128 v[192:195], v188 offset:32768
	ds_read_b128 v[196:199], v188 offset:33792
	ds_read_b128 v[200:203], v188 offset:34816
	ds_read_b128 v[204:207], v188 offset:35840
	ds_read_b128 v[216:219], v188 offset:36864
	ds_read_b128 v[220:223], v188 offset:37888
	ds_read_b128 v[224:227], v188 offset:38912
	ds_read_b128 v[228:231], v188 offset:39936
	global_load_lds_dwordx4 v[208:209], off
	v_lshl_add_u64 v[208:209], s[38:39], 0, v[164:165]
	s_mov_b32 m0, s49
	s_nop 0
	global_load_lds_dwordx4 v[208:209], off
	s_waitcnt vmcnt(8)
	s_waitcnt lgkmcnt(0)
	s_setprio 1
	s_barrier
	v_mfma_scale_f32_16x16x128_f8f6f4 v[158:161], v[2:9], v[192:199], v[158:161], v189, v190 op_sel_hi:[0,0,0]
	v_mfma_scale_f32_16x16x128_f8f6f4 v[150:153], v[10:17], v[192:199], v[150:153], v189, v190 op_sel_hi:[0,0,0]
	v_mfma_scale_f32_16x16x128_f8f6f4 v[142:145], v[2:9], v[200:207], v[142:145], v189, v190 op_sel_hi:[0,0,0]
	v_mfma_scale_f32_16x16x128_f8f6f4 v[134:137], v[10:17], v[200:207], v[134:137], v189, v190 op_sel_hi:[0,0,0]
	v_mfma_scale_f32_16x16x128_f8f6f4 v[126:129], v[2:9], v[216:223], v[126:129], v189, v190 op_sel_hi:[0,0,0]
	v_mfma_scale_f32_16x16x128_f8f6f4 v[118:121], v[10:17], v[216:223], v[118:121], v189, v190 op_sel_hi:[0,0,0]
	v_mfma_scale_f32_16x16x128_f8f6f4 v[110:113], v[2:9], v[224:231], v[110:113], v189, v190 op_sel_hi:[0,0,0]
	v_mfma_scale_f32_16x16x128_f8f6f4 v[102:105], v[10:17], v[224:231], v[102:105], v189, v190 op_sel_hi:[0,0,0]
	s_setprio 0
	s_setprio 1
	v_mfma_scale_f32_16x16x128_f8f6f4 v[154:157], v[18:25], v[192:199], v[154:157], v189, v190 op_sel_hi:[0,0,0]
	v_mfma_scale_f32_16x16x128_f8f6f4 v[146:149], v[26:33], v[192:199], v[146:149], v189, v190 op_sel_hi:[0,0,0]
	v_mfma_scale_f32_16x16x128_f8f6f4 v[138:141], v[18:25], v[200:207], v[138:141], v189, v190 op_sel_hi:[0,0,0]
	v_mfma_scale_f32_16x16x128_f8f6f4 v[130:133], v[26:33], v[200:207], v[130:133], v189, v190 op_sel_hi:[0,0,0]
	v_mfma_scale_f32_16x16x128_f8f6f4 v[122:125], v[18:25], v[216:223], v[122:125], v189, v190 op_sel_hi:[0,0,0]
	v_mfma_scale_f32_16x16x128_f8f6f4 v[114:117], v[26:33], v[216:223], v[114:117], v189, v190 op_sel_hi:[0,0,0]
	v_mfma_scale_f32_16x16x128_f8f6f4 v[106:109], v[18:25], v[224:231], v[106:109], v189, v190 op_sel_hi:[0,0,0]
	v_mfma_scale_f32_16x16x128_f8f6f4 v[98:101], v[26:33], v[224:231], v[98:101], v189, v190 op_sel_hi:[0,0,0]
	s_barrier
	s_setprio 0
	s_add_i32 s38, s71, s43
	v_lshl_add_u64 v[176:177], v[176:177], 0, s[12:13]
	s_mov_b32 m0, s38
	ds_read_b128 v[192:195], v188 offset:49152
	ds_read_b128 v[196:199], v188 offset:50176
	ds_read_b128 v[200:203], v188 offset:51200
	ds_read_b128 v[204:207], v188 offset:52224
	ds_read_b128 v[216:219], v188 offset:53248
	ds_read_b128 v[220:223], v188 offset:54272
	ds_read_b128 v[224:227], v188 offset:55296
	ds_read_b128 v[228:231], v188 offset:56320
	global_load_lds_dwordx4 v[176:177], off
	s_add_i32 m0, s38, 0x2000
	s_add_u32 s36, s36, 0x40080
	v_lshl_add_u64 v[176:177], v[178:179], 0, s[12:13]
	s_addc_u32 s37, s37, 0
	s_add_i32 s38, s72, s43
	global_load_lds_dwordx4 v[176:177], off
	v_lshl_add_u64 v[176:177], s[36:37], 0, v[166:167]
	s_mov_b32 m0, s38
	s_nop 0
	global_load_lds_dwordx4 v[176:177], off
	v_lshl_add_u64 v[176:177], s[36:37], 0, v[162:163]
	s_add_i32 m0, s38, 0x2000
	s_nop 0
	global_load_lds_dwordx4 v[176:177], off
	v_lshl_add_u64 v[176:177], v[180:181], 0, s[12:13]
	s_mov_b32 m0, s50
	s_nop 0
	global_load_lds_dwordx4 v[176:177], off
	v_lshl_add_u64 v[176:177], v[182:183], 0, s[12:13]
	s_mov_b32 m0, s51
	s_nop 0
	global_load_lds_dwordx4 v[176:177], off
	s_waitcnt vmcnt(8)
	s_waitcnt lgkmcnt(0)
	s_setprio 1
	s_barrier
	v_mfma_scale_f32_16x16x128_f8f6f4 v[94:97], v[2:9], v[192:199], v[94:97], v189, v190 op_sel_hi:[0,0,0]
	v_mfma_scale_f32_16x16x128_f8f6f4 v[86:89], v[10:17], v[192:199], v[86:89], v189, v190 op_sel_hi:[0,0,0]
	v_mfma_scale_f32_16x16x128_f8f6f4 v[78:81], v[2:9], v[200:207], v[78:81], v189, v190 op_sel_hi:[0,0,0]
	v_mfma_scale_f32_16x16x128_f8f6f4 v[70:73], v[10:17], v[200:207], v[70:73], v189, v190 op_sel_hi:[0,0,0]
	v_mfma_scale_f32_16x16x128_f8f6f4 v[62:65], v[2:9], v[216:223], v[62:65], v189, v190 op_sel_hi:[0,0,0]
	v_mfma_scale_f32_16x16x128_f8f6f4 v[54:57], v[10:17], v[216:223], v[54:57], v189, v190 op_sel_hi:[0,0,0]
	v_mfma_scale_f32_16x16x128_f8f6f4 v[46:49], v[2:9], v[224:231], v[46:49], v189, v190 op_sel_hi:[0,0,0]
	v_mfma_scale_f32_16x16x128_f8f6f4 v[38:41], v[10:17], v[224:231], v[38:41], v189, v190 op_sel_hi:[0,0,0]
	s_setprio 0
	s_setprio 1
	v_mfma_scale_f32_16x16x128_f8f6f4 v[90:93], v[18:25], v[192:199], v[90:93], v189, v190 op_sel_hi:[0,0,0]
	v_mfma_scale_f32_16x16x128_f8f6f4 v[82:85], v[26:33], v[192:199], v[82:85], v189, v190 op_sel_hi:[0,0,0]
	v_mfma_scale_f32_16x16x128_f8f6f4 v[74:77], v[18:25], v[200:207], v[74:77], v189, v190 op_sel_hi:[0,0,0]
	v_mfma_scale_f32_16x16x128_f8f6f4 v[66:69], v[26:33], v[200:207], v[66:69], v189, v190 op_sel_hi:[0,0,0]
	v_mfma_scale_f32_16x16x128_f8f6f4 v[58:61], v[18:25], v[216:223], v[58:61], v189, v190 op_sel_hi:[0,0,0]
	v_mfma_scale_f32_16x16x128_f8f6f4 v[50:53], v[26:33], v[216:223], v[50:53], v189, v190 op_sel_hi:[0,0,0]
	v_mfma_scale_f32_16x16x128_f8f6f4 v[42:45], v[18:25], v[224:231], v[42:45], v189, v190 op_sel_hi:[0,0,0]
	v_mfma_scale_f32_16x16x128_f8f6f4 v[34:37], v[26:33], v[224:231], v[34:37], v189, v190 op_sel_hi:[0,0,0]
	s_barrier
	s_setprio 0
	s_add_i32 s70, s70, 2
	s_add_u32 s34, s34, 0x100
	s_addc_u32 s35, s35, 0
	s_add_u32 s68, s68, 0x100
	s_addc_u32 s69, s69, 0
	s_cmp_gt_u32 s70, 13
	s_cbranch_scc0 .LBB0_2366
	s_and_b64 vcc, exec, s[16:17]
	s_cbranch_vccz .LBB0_2369
	s_barrier

.LBB0_2441:
	ds_read_b128 v[16:19], v191
	ds_read_b128 v[20:23], v191 offset:1024
	ds_read_b128 v[24:27], v191 offset:2048
	ds_read_b128 v[28:31], v191 offset:3072
	ds_read_b128 v[0:3], v192
	ds_read_b128 v[4:7], v192 offset:1024
	ds_read_b128 v[8:11], v192 offset:2048
	ds_read_b128 v[12:15], v192 offset:3072
	s_add_u32 s40, s38, 0xfff20080
	s_addc_u32 s41, s39, -1
	s_cmp_eq_u32 s71, 52
	s_cselect_b64 vcc, -1, 0
	s_cselect_b32 s41, s1, s41
	s_cselect_b32 s40, s0, s40
	v_cndmask_b32_e32 v179, v177, v175, vcc
	v_cndmask_b32_e32 v178, v176, v174, vcc
	v_lshl_add_u64 v[214:215], s[38:39], 0, v[168:169]
	s_add_i32 m0, s47, 0xc000
	ds_read_b128 v[180:183], v193
	ds_read_b128 v[184:187], v193 offset:1024
	ds_read_b128 v[198:201], v193 offset:2048
	ds_read_b128 v[202:205], v193 offset:3072
	ds_read_b128 v[206:209], v193 offset:4096
	ds_read_b128 v[210:213], v193 offset:5120
	ds_read_b128 v[216:219], v193 offset:6144
	ds_read_b128 v[220:223], v193 offset:7168
	global_load_lds_dwordx4 v[214:215], off
	v_lshl_add_u64 v[214:215], s[38:39], 0, v[170:171]
	s_add_i32 m0, s47, 0xe000
	s_nop 0
	global_load_lds_dwordx4 v[214:215], off
	s_waitcnt vmcnt(8)
	s_waitcnt lgkmcnt(0)
	s_setprio 1
	s_barrier
	v_mfma_scale_f32_16x16x128_f8f6f4 v[156:159], v[16:23], v[180:187], v[156:159], v194, v195 op_sel_hi:[0,0,0]
	v_mfma_scale_f32_16x16x128_f8f6f4 v[152:155], v[24:31], v[180:187], v[152:155], v194, v195 op_sel_hi:[0,0,0]
	v_mfma_scale_f32_16x16x128_f8f6f4 v[148:151], v[16:23], v[198:205], v[148:151], v194, v195 op_sel_hi:[0,0,0]
	v_mfma_scale_f32_16x16x128_f8f6f4 v[140:143], v[24:31], v[198:205], v[140:143], v194, v195 op_sel_hi:[0,0,0]
	v_mfma_scale_f32_16x16x128_f8f6f4 v[132:135], v[16:23], v[206:213], v[132:135], v194, v195 op_sel_hi:[0,0,0]
	v_mfma_scale_f32_16x16x128_f8f6f4 v[124:127], v[24:31], v[206:213], v[124:127], v194, v195 op_sel_hi:[0,0,0]
	v_mfma_scale_f32_16x16x128_f8f6f4 v[116:119], v[16:23], v[216:223], v[116:119], v194, v195 op_sel_hi:[0,0,0]
	v_mfma_scale_f32_16x16x128_f8f6f4 v[108:111], v[24:31], v[216:223], v[108:111], v194, v195 op_sel_hi:[0,0,0]
	s_setprio 0
	s_setprio 1
	v_mfma_scale_f32_16x16x128_f8f6f4 v[144:147], v[0:7], v[180:187], v[144:147], v194, v195 op_sel_hi:[0,0,0]
	v_mfma_scale_f32_16x16x128_f8f6f4 v[136:139], v[8:15], v[180:187], v[136:139], v194, v195 op_sel_hi:[0,0,0]
	v_mfma_scale_f32_16x16x128_f8f6f4 v[128:131], v[0:7], v[198:205], v[128:131], v194, v195 op_sel_hi:[0,0,0]
	v_mfma_scale_f32_16x16x128_f8f6f4 v[120:123], v[8:15], v[198:205], v[120:123], v194, v195 op_sel_hi:[0,0,0]
	v_mfma_scale_f32_16x16x128_f8f6f4 v[112:115], v[0:7], v[206:213], v[112:115], v194, v195 op_sel_hi:[0,0,0]
	v_mfma_scale_f32_16x16x128_f8f6f4 v[104:107], v[8:15], v[206:213], v[104:107], v194, v195 op_sel_hi:[0,0,0]
	v_mfma_scale_f32_16x16x128_f8f6f4 v[100:103], v[0:7], v[216:223], v[100:103], v194, v195 op_sel_hi:[0,0,0]
	v_mfma_scale_f32_16x16x128_f8f6f4 v[96:99], v[8:15], v[216:223], v[96:99], v194, v195 op_sel_hi:[0,0,0]
	s_barrier
	s_setprio 0
	s_add_i32 s72, s6, s44
	v_lshl_add_u64 v[180:181], v[178:179], 0, v[164:165]
	s_mov_b32 m0, s72
	ds_read_b128 v[198:201], v193 offset:16384
	ds_read_b128 v[202:205], v193 offset:17408
	ds_read_b128 v[206:209], v193 offset:18432
	ds_read_b128 v[210:213], v193 offset:19456
	ds_read_b128 v[216:219], v193 offset:20480
	ds_read_b128 v[220:223], v193 offset:21504
	ds_read_b128 v[224:227], v193 offset:22528
	ds_read_b128 v[228:231], v193 offset:23552
	global_load_lds_dwordx4 v[180:181], off
	v_lshl_add_u64 v[182:183], v[178:179], 0, v[160:161]
	s_add_i32 m0, s72, 0x2000
	v_lshl_add_u64 v[184:185], v[178:179], 0, s[10:11]
	s_add_i32 s72, s62, s44
	global_load_lds_dwordx4 v[182:183], off
	v_lshl_add_u64 v[186:187], v[184:185], 0, v[164:165]
	s_mov_b32 m0, s72
	v_lshl_add_u64 v[184:185], v[184:185], 0, v[160:161]
	global_load_lds_dwordx4 v[186:187], off
	s_add_i32 m0, s72, 0x2000
	v_lshl_add_u64 v[186:187], s[40:41], 0, v[162:163]
	global_load_lds_dwordx4 v[184:185], off
	v_lshl_add_u64 v[184:185], s[40:41], 0, v[166:167]
	s_mov_b32 m0, s47
	s_nop 0
	global_load_lds_dwordx4 v[184:185], off
	s_mov_b32 m0, s48
	s_nop 0
	global_load_lds_dwordx4 v[186:187], off
	s_waitcnt vmcnt(8)
	s_waitcnt lgkmcnt(0)
	s_setprio 1
	s_barrier
	v_mfma_scale_f32_16x16x128_f8f6f4 v[92:95], v[16:23], v[198:205], v[92:95], v194, v195 op_sel_hi:[0,0,0]
	v_mfma_scale_f32_16x16x128_f8f6f4 v[88:91], v[24:31], v[198:205], v[88:91], v194, v195 op_sel_hi:[0,0,0]
	v_mfma_scale_f32_16x16x128_f8f6f4 v[84:87], v[16:23], v[206:213], v[84:87], v194, v195 op_sel_hi:[0,0,0]
	v_mfma_scale_f32_16x16x128_f8f6f4 v[76:79], v[24:31], v[206:213], v[76:79], v194, v195 op_sel_hi:[0,0,0]
	v_mfma_scale_f32_16x16x128_f8f6f4 v[68:71], v[16:23], v[216:223], v[68:71], v194, v195 op_sel_hi:[0,0,0]
	v_mfma_scale_f32_16x16x128_f8f6f4 v[60:63], v[24:31], v[216:223], v[60:63], v194, v195 op_sel_hi:[0,0,0]
	v_mfma_scale_f32_16x16x128_f8f6f4 v[52:55], v[16:23], v[224:231], v[52:55], v194, v195 op_sel_hi:[0,0,0]
	v_mfma_scale_f32_16x16x128_f8f6f4 v[44:47], v[24:31], v[224:231], v[44:47], v194, v195 op_sel_hi:[0,0,0]
	s_setprio 0
	s_setprio 1
	v_mfma_scale_f32_16x16x128_f8f6f4 v[80:83], v[0:7], v[198:205], v[80:83], v194, v195 op_sel_hi:[0,0,0]
	v_mfma_scale_f32_16x16x128_f8f6f4 v[72:75], v[8:15], v[198:205], v[72:75], v194, v195 op_sel_hi:[0,0,0]
	v_mfma_scale_f32_16x16x128_f8f6f4 v[64:67], v[0:7], v[206:213], v[64:67], v194, v195 op_sel_hi:[0,0,0]
	v_mfma_scale_f32_16x16x128_f8f6f4 v[56:59], v[8:15], v[206:213], v[56:59], v194, v195 op_sel_hi:[0,0,0]
	v_mfma_scale_f32_16x16x128_f8f6f4 v[48:51], v[0:7], v[216:223], v[48:51], v194, v195 op_sel_hi:[0,0,0]
	v_mfma_scale_f32_16x16x128_f8f6f4 v[40:43], v[8:15], v[216:223], v[40:43], v194, v195 op_sel_hi:[0,0,0]
	v_mfma_scale_f32_16x16x128_f8f6f4 v[36:39], v[0:7], v[224:231], v[36:39], v194, v195 op_sel_hi:[0,0,0]
	v_mfma_scale_f32_16x16x128_f8f6f4 v[32:35], v[8:15], v[224:231], v[32:35], v194, v195 op_sel_hi:[0,0,0]
	s_barrier
	s_setprio 0
	s_add_i32 s72, 0, 0x18000
	s_add_i32 s73, 0, 0x1c000
	v_add_u32_e32 v12, s72, v189
	v_add_u32_e32 v28, s73, v189
	ds_read_b128 v[0:3], v12
	ds_read_b128 v[4:7], v12 offset:1024
	ds_read_b128 v[8:11], v12 offset:2048
	ds_read_b128 v[12:15], v12 offset:3072
	ds_read_b128 v[16:19], v28
	ds_read_b128 v[20:23], v28 offset:1024
	ds_read_b128 v[24:27], v28 offset:2048
	ds_read_b128 v[28:31], v28 offset:3072
	s_add_u32 s40, s40, 0xe0000
	s_addc_u32 s41, s41, 0
	s_mov_b32 m0, s49
	v_lshl_add_u64 v[214:215], s[40:41], 0, v[166:167]
	ds_read_b128 v[198:201], v193 offset:32768
	ds_read_b128 v[202:205], v193 offset:33792
	ds_read_b128 v[206:209], v193 offset:34816
	ds_read_b128 v[210:213], v193 offset:35840
	ds_read_b128 v[216:219], v193 offset:36864
	ds_read_b128 v[220:223], v193 offset:37888
	ds_read_b128 v[224:227], v193 offset:38912
	ds_read_b128 v[228:231], v193 offset:39936
	global_load_lds_dwordx4 v[214:215], off
	v_lshl_add_u64 v[214:215], s[40:41], 0, v[162:163]
	s_mov_b32 m0, s50
	s_nop 0
	global_load_lds_dwordx4 v[214:215], off
	s_waitcnt vmcnt(8)
	s_waitcnt lgkmcnt(0)
	s_setprio 1
	s_barrier
	v_mfma_scale_f32_16x16x128_f8f6f4 v[156:159], v[0:7], v[198:205], v[156:159], v194, v195 op_sel_hi:[0,0,0]
	v_mfma_scale_f32_16x16x128_f8f6f4 v[152:155], v[8:15], v[198:205], v[152:155], v194, v195 op_sel_hi:[0,0,0]
	v_mfma_scale_f32_16x16x128_f8f6f4 v[148:151], v[0:7], v[206:213], v[148:151], v194, v195 op_sel_hi:[0,0,0]
	v_mfma_scale_f32_16x16x128_f8f6f4 v[140:143], v[8:15], v[206:213], v[140:143], v194, v195 op_sel_hi:[0,0,0]
	v_mfma_scale_f32_16x16x128_f8f6f4 v[132:135], v[0:7], v[216:223], v[132:135], v194, v195 op_sel_hi:[0,0,0]
	v_mfma_scale_f32_16x16x128_f8f6f4 v[124:127], v[8:15], v[216:223], v[124:127], v194, v195 op_sel_hi:[0,0,0]
	v_mfma_scale_f32_16x16x128_f8f6f4 v[116:119], v[0:7], v[224:231], v[116:119], v194, v195 op_sel_hi:[0,0,0]
	v_mfma_scale_f32_16x16x128_f8f6f4 v[108:111], v[8:15], v[224:231], v[108:111], v194, v195 op_sel_hi:[0,0,0]
	s_setprio 0
	s_setprio 1
	v_mfma_scale_f32_16x16x128_f8f6f4 v[144:147], v[16:23], v[198:205], v[144:147], v194, v195 op_sel_hi:[0,0,0]
	v_mfma_scale_f32_16x16x128_f8f6f4 v[136:139], v[24:31], v[198:205], v[136:139], v194, v195 op_sel_hi:[0,0,0]
	v_mfma_scale_f32_16x16x128_f8f6f4 v[128:131], v[16:23], v[206:213], v[128:131], v194, v195 op_sel_hi:[0,0,0]
	v_mfma_scale_f32_16x16x128_f8f6f4 v[120:123], v[24:31], v[206:213], v[120:123], v194, v195 op_sel_hi:[0,0,0]
	v_mfma_scale_f32_16x16x128_f8f6f4 v[112:115], v[16:23], v[216:223], v[112:115], v194, v195 op_sel_hi:[0,0,0]
	v_mfma_scale_f32_16x16x128_f8f6f4 v[104:107], v[24:31], v[216:223], v[104:107], v194, v195 op_sel_hi:[0,0,0]
	v_mfma_scale_f32_16x16x128_f8f6f4 v[100:103], v[16:23], v[224:231], v[100:103], v194, v195 op_sel_hi:[0,0,0]
	v_mfma_scale_f32_16x16x128_f8f6f4 v[96:99], v[24:31], v[224:231], v[96:99], v194, v195 op_sel_hi:[0,0,0]
	s_barrier
	s_setprio 0
	s_add_i32 s40, s72, s44
	v_lshl_add_u64 v[180:181], v[180:181], 0, s[18:19]
	s_mov_b32 m0, s40
	ds_read_b128 v[198:201], v193 offset:49152
	ds_read_b128 v[202:205], v193 offset:50176
	ds_read_b128 v[206:209], v193 offset:51200
	ds_read_b128 v[210:213], v193 offset:52224
	ds_read_b128 v[216:219], v193 offset:53248
	ds_read_b128 v[220:223], v193 offset:54272
	ds_read_b128 v[224:227], v193 offset:55296
	ds_read_b128 v[228:231], v193 offset:56320
	global_load_lds_dwordx4 v[180:181], off
	v_lshl_add_u64 v[180:181], v[182:183], 0, s[18:19]
	s_add_i32 m0, s40, 0x2000
	v_lshl_add_u64 v[178:179], v[178:179], 0, s[22:23]
	s_add_i32 s40, s73, s44
	global_load_lds_dwordx4 v[180:181], off
	v_lshl_add_u64 v[180:181], v[178:179], 0, v[164:165]
	s_mov_b32 m0, s40
	v_lshl_add_u64 v[178:179], v[178:179], 0, v[160:161]
	global_load_lds_dwordx4 v[180:181], off
	s_add_i32 m0, s40, 0x2000
	s_nop 0
	global_load_lds_dwordx4 v[178:179], off
	v_lshl_add_u64 v[178:179], v[184:185], 0, s[18:19]
	s_mov_b32 m0, s59
	s_nop 0
	global_load_lds_dwordx4 v[178:179], off
	v_lshl_add_u64 v[178:179], v[186:187], 0, s[18:19]
	s_mov_b32 m0, s60
	s_nop 0
	global_load_lds_dwordx4 v[178:179], off
	s_waitcnt vmcnt(8)
	s_waitcnt lgkmcnt(0)
	s_setprio 1
	s_barrier
	v_mfma_scale_f32_16x16x128_f8f6f4 v[92:95], v[0:7], v[198:205], v[92:95], v194, v195 op_sel_hi:[0,0,0]
	v_mfma_scale_f32_16x16x128_f8f6f4 v[88:91], v[8:15], v[198:205], v[88:91], v194, v195 op_sel_hi:[0,0,0]
	v_mfma_scale_f32_16x16x128_f8f6f4 v[84:87], v[0:7], v[206:213], v[84:87], v194, v195 op_sel_hi:[0,0,0]
	v_mfma_scale_f32_16x16x128_f8f6f4 v[76:79], v[8:15], v[206:213], v[76:79], v194, v195 op_sel_hi:[0,0,0]
	v_mfma_scale_f32_16x16x128_f8f6f4 v[68:71], v[0:7], v[216:223], v[68:71], v194, v195 op_sel_hi:[0,0,0]
	v_mfma_scale_f32_16x16x128_f8f6f4 v[60:63], v[8:15], v[216:223], v[60:63], v194, v195 op_sel_hi:[0,0,0]
	v_mfma_scale_f32_16x16x128_f8f6f4 v[52:55], v[0:7], v[224:231], v[52:55], v194, v195 op_sel_hi:[0,0,0]
	v_mfma_scale_f32_16x16x128_f8f6f4 v[44:47], v[8:15], v[224:231], v[44:47], v194, v195 op_sel_hi:[0,0,0]
	s_setprio 0
	s_setprio 1
	v_mfma_scale_f32_16x16x128_f8f6f4 v[80:83], v[16:23], v[198:205], v[80:83], v194, v195 op_sel_hi:[0,0,0]
	v_mfma_scale_f32_16x16x128_f8f6f4 v[72:75], v[24:31], v[198:205], v[72:75], v194, v195 op_sel_hi:[0,0,0]
	v_mfma_scale_f32_16x16x128_f8f6f4 v[64:67], v[16:23], v[206:213], v[64:67], v194, v195 op_sel_hi:[0,0,0]
	v_mfma_scale_f32_16x16x128_f8f6f4 v[56:59], v[24:31], v[206:213], v[56:59], v194, v195 op_sel_hi:[0,0,0]
	v_mfma_scale_f32_16x16x128_f8f6f4 v[48:51], v[16:23], v[216:223], v[48:51], v194, v195 op_sel_hi:[0,0,0]
	v_mfma_scale_f32_16x16x128_f8f6f4 v[40:43], v[24:31], v[216:223], v[40:43], v194, v195 op_sel_hi:[0,0,0]
	v_mfma_scale_f32_16x16x128_f8f6f4 v[36:39], v[16:23], v[224:231], v[36:39], v194, v195 op_sel_hi:[0,0,0]
	v_mfma_scale_f32_16x16x128_f8f6f4 v[32:35], v[24:31], v[224:231], v[32:35], v194, v195 op_sel_hi:[0,0,0]
	s_barrier
	s_setprio 0
	s_add_i32 s71, s71, 2
	s_add_u32 s38, s38, 0x100
	s_addc_u32 s39, s39, 0
	s_cmp_gt_u32 s71, 53
	v_lshl_add_u64 v[176:177], v[176:177], 0, s[26:27]
	s_cbranch_scc0 .LBB0_2441
	s_and_b64 vcc, exec, s[24:25]
	s_cbranch_vccz .LBB0_2444
	s_barrier
